# baseline (speedup 1.0000x reference)
_Z10scan_pass2PKDF16_PKfS2_S0_S2_S0_PDF16_S2_:
	s_load_dwordx16 s[8:23], s[0:1], 0x0
	s_mov_b32 s28, 0x3b800000
	s_mov_b32 s29, 0x3c800000
	s_mov_b32 s30, 0x43800000
	s_lshl_b32 s5, s4, 11
	s_lshl_b32 s6, s3, 5
	s_add_i32 s5, s5, s6
	s_lshl_b32 s6, s4, 6
	s_add_i32 s6, s6, s3
	v_lshl_or_b32 v1, s2, 8, v0
	v_lshlrev_b32_e32 v99, 1, v1
	v_lshlrev_b32_e32 v100, 6, v1
	v_lshlrev_b32_e32 v101, 2, v1
	v_lshlrev_b32_e32 v102, 4, v1
	v_lshlrev_b32_e32 v103, 3, v1
	s_waitcnt lgkmcnt(0)
	s_lshl_b32 s7, s5, 7
	s_add_u32 s24, s10, s7
	s_addc_u32 s25, s11, 0
	s_load_dwordx16 s[32:47], s[24:25], 0x0
	s_load_dwordx16 s[48:63], s[24:25], 0x40
	global_load_dwordx4 v[2:5], v100, s[12:13]
	global_load_dwordx4 v[6:9], v100, s[12:13] offset:16
	global_load_dwordx4 v[10:13], v100, s[12:13] offset:32
	global_load_dwordx4 v[14:17], v100, s[12:13] offset:48
	s_lshl_b32 s7, s6, 16
	s_add_u32 s96, s14, s7
	s_addc_u32 s97, s15, 0
	global_load_dword v104, v101, s[96:97]
	s_add_u32 s96, s96, 0x2000
	s_addc_u32 s97, s97, 0
	global_load_dword v105, v101, s[96:97]
	s_add_u32 s96, s96, 0x2000
	s_addc_u32 s97, s97, 0
	global_load_dword v106, v101, s[96:97]
	s_add_u32 s96, s96, 0x2000
	s_addc_u32 s97, s97, 0
	global_load_dword v107, v101, s[96:97]
	s_add_u32 s96, s96, 0x2000
	s_addc_u32 s97, s97, 0
	global_load_dword v108, v101, s[96:97]
	s_add_u32 s96, s96, 0x2000
	s_addc_u32 s97, s97, 0
	global_load_dword v109, v101, s[96:97]
	s_add_u32 s96, s96, 0x2000
	s_addc_u32 s97, s97, 0
	global_load_dword v110, v101, s[96:97]
	s_add_u32 s96, s96, 0x2000
	s_addc_u32 s97, s97, 0
	global_load_dword v111, v101, s[96:97]
	s_lshr_b32 s7, s5, 2
	s_lshl_b32 s7, s7, 15
	s_add_u32 s0, s22, s7
	s_addc_u32 s1, s23, 0
	s_add_u32 s2, s18, s7
	s_addc_u32 s3, s19, 0
	s_add_u32 s2, s2, 0x4000
	s_addc_u32 s3, s3, 0
	s_lshr_b32 s7, s5, 3
	s_lshl_b32 s7, s7, 15
	s_add_u32 s8, s8, s7
	s_addc_u32 s9, s9, 0
	s_lshl_b32 s7, s5, 12
	s_add_u32 s26, s20, s7
	s_addc_u32 s27, s21, 0
	global_load_dwordx4 v[34:37], v102, s[0:1]
	s_add_u32 s0, s0, 0x8000
	s_addc_u32 s1, s1, 0
	global_load_dwordx4 v[42:45], v102, s[8:9]
	s_add_u32 s8, s8, 0x8000
	s_addc_u32 s9, s9, 0
	global_load_dwordx2 v[46:47], v103, s[2:3]
	s_add_u32 s2, s2, 0x8000
	s_addc_u32 s3, s3, 0
	global_load_dwordx4 v[38:41], v102, s[0:1]
	s_add_u32 s0, s0, 0x8000
	s_addc_u32 s1, s1, 0
	global_load_dwordx2 v[48:49], v103, s[2:3]
	s_add_u32 s2, s2, 0x8000
	s_addc_u32 s3, s3, 0
	global_load_dword v98, v101, s[16:17]
	global_load_dwordx4 v[50:53], v102, s[0:1]
	s_add_u32 s0, s0, 0x8000
	s_addc_u32 s1, s1, 0
	global_load_dwordx4 v[58:61], v102, s[8:9]
	s_add_u32 s8, s8, 0x8000
	s_addc_u32 s9, s9, 0
	global_load_dwordx2 v[62:63], v103, s[2:3]
	s_add_u32 s2, s2, 0x8000
	s_addc_u32 s3, s3, 0
	global_load_dwordx4 v[54:57], v102, s[0:1]
	s_add_u32 s0, s0, 0x8000
	s_addc_u32 s1, s1, 0
	global_load_dwordx2 v[64:65], v103, s[2:3]
	s_add_u32 s2, s2, 0x8000
	s_addc_u32 s3, s3, 0
	s_waitcnt vmcnt(11)
	v_cvt_f32_f16_e32 v18, v104
	v_cvt_f32_f16_sdwa v19, v104 dst_sel:DWORD dst_unused:UNUSED_PAD src0_sel:WORD_1
	v_cvt_f32_f16_e32 v20, v105
	v_cvt_f32_f16_sdwa v21, v105 dst_sel:DWORD dst_unused:UNUSED_PAD src0_sel:WORD_1
	v_cvt_f32_f16_e32 v22, v106
	v_cvt_f32_f16_sdwa v23, v106 dst_sel:DWORD dst_unused:UNUSED_PAD src0_sel:WORD_1
	v_cvt_f32_f16_e32 v24, v107
	v_cvt_f32_f16_sdwa v25, v107 dst_sel:DWORD dst_unused:UNUSED_PAD src0_sel:WORD_1
	v_cvt_f32_f16_e32 v26, v108
	v_cvt_f32_f16_sdwa v27, v108 dst_sel:DWORD dst_unused:UNUSED_PAD src0_sel:WORD_1
	v_cvt_f32_f16_e32 v28, v109
	v_cvt_f32_f16_sdwa v29, v109 dst_sel:DWORD dst_unused:UNUSED_PAD src0_sel:WORD_1
	v_cvt_f32_f16_e32 v30, v110
	v_cvt_f32_f16_sdwa v31, v110 dst_sel:DWORD dst_unused:UNUSED_PAD src0_sel:WORD_1
	v_cvt_f32_f16_e32 v32, v111
	v_cvt_f32_f16_sdwa v33, v111 dst_sel:DWORD dst_unused:UNUSED_PAD src0_sel:WORD_1
	v_pk_mul_f32 v[18:19], v[18:19], s[28:29] op_sel_hi:[1,0]
	v_pk_mul_f32 v[20:21], v[20:21], s[28:29] op_sel_hi:[1,0]
	v_pk_mul_f32 v[22:23], v[22:23], s[28:29] op_sel_hi:[1,0]
	v_pk_mul_f32 v[24:25], v[24:25], s[28:29] op_sel_hi:[1,0]
	v_pk_mul_f32 v[26:27], v[26:27], s[28:29] op_sel_hi:[1,0]
	v_pk_mul_f32 v[28:29], v[28:29], s[28:29] op_sel_hi:[1,0]
	v_pk_mul_f32 v[30:31], v[30:31], s[28:29] op_sel_hi:[1,0]
	v_pk_mul_f32 v[32:33], v[32:33], s[28:29] op_sel_hi:[1,0]
	s_waitcnt vmcnt(5)
	global_load_dwordx4 v[66:69], v102, s[0:1]
	s_add_u32 s0, s0, 0x8000
	s_addc_u32 s1, s1, 0
	global_load_dwordx4 v[74:77], v102, s[8:9]
	s_add_u32 s8, s8, 0x8000
	s_addc_u32 s9, s9, 0
	global_load_dwordx2 v[78:79], v103, s[2:3]
	s_add_u32 s2, s2, 0x8000
	s_addc_u32 s3, s3, 0
	global_load_dwordx4 v[70:73], v102, s[0:1]
	s_add_u32 s0, s0, 0x8000
	s_addc_u32 s1, s1, 0
	global_load_dwordx2 v[80:81], v103, s[2:3]
	s_add_u32 s2, s2, 0x8000
	s_addc_u32 s3, s3, 0
	s_waitcnt lgkmcnt(0)
	s_load_dwordx16 s[64:79], s[24:25], 0x80
	s_load_dwordx16 s[80:95], s[24:25], 0xc0
	v_cvt_f32_f16_e32 v113, v42
	v_mul_f32_e32 v113, s29, v113
	v_mul_f32_e32 v112, v34, v113
	v_pk_mul_f32 v[104:105], v[34:35], v[2:3] op_sel_hi:[0,1]
	v_pk_mul_f32 v[106:107], v[34:35], v[4:5] op_sel_hi:[0,1]
	v_exp_f32_e32 v104, v104
	v_exp_f32_e32 v105, v105
	v_exp_f32_e32 v106, v106
	v_pk_mul_f32 v[104:105], v[18:19], v[104:105]
	v_exp_f32_e32 v107, v107
	v_pk_fma_f32 v[18:19], v[112:113], s[32:33], v[104:105] op_sel_hi:[0,1,1]
	v_pk_mul_f32 v[106:107], v[20:21], v[106:107]
	v_pk_fma_f32 v[114:115], s[48:49], v[18:19], 0 op_sel_hi:[1,1,0]
	v_pk_fma_f32 v[20:21], v[112:113], s[34:35], v[106:107] op_sel_hi:[0,1,1]
	v_pk_mul_f32 v[108:109], v[34:35], v[6:7] op_sel_hi:[0,1]
	v_pk_fma_f32 v[114:115], s[50:51], v[20:21], v[114:115]
	v_exp_f32_e32 v108, v108
	v_exp_f32_e32 v109, v109
	v_pk_mul_f32 v[110:111], v[34:35], v[8:9] op_sel_hi:[0,1]
	v_pk_mul_f32 v[108:109], v[22:23], v[108:109]
	v_exp_f32_e32 v110, v110
	v_pk_fma_f32 v[22:23], v[112:113], s[36:37], v[108:109] op_sel_hi:[0,1,1]
	v_exp_f32_e32 v111, v111
	v_pk_fma_f32 v[114:115], s[52:53], v[22:23], v[114:115]
	v_pk_mul_f32 v[110:111], v[24:25], v[110:111]
	v_pk_mul_f32 v[104:105], v[34:35], v[10:11] op_sel_hi:[0,1]
	v_pk_fma_f32 v[24:25], v[112:113], s[38:39], v[110:111] op_sel_hi:[0,1,1]
	v_exp_f32_e32 v104, v104
	v_pk_fma_f32 v[114:115], s[54:55], v[24:25], v[114:115]
	v_exp_f32_e32 v105, v105
	v_pk_mul_f32 v[106:107], v[34:35], v[12:13] op_sel_hi:[0,1]
	v_pk_mul_f32 v[104:105], v[26:27], v[104:105]
	v_exp_f32_e32 v106, v106
	v_pk_fma_f32 v[26:27], v[112:113], s[40:41], v[104:105] op_sel_hi:[0,1,1]
	v_exp_f32_e32 v107, v107
	v_pk_fma_f32 v[114:115], s[56:57], v[26:27], v[114:115]
	v_pk_mul_f32 v[106:107], v[28:29], v[106:107]
	v_pk_mul_f32 v[108:109], v[34:35], v[14:15] op_sel_hi:[0,1]
	v_pk_fma_f32 v[28:29], v[112:113], s[42:43], v[106:107] op_sel_hi:[0,1,1]
	v_exp_f32_e32 v108, v108
	v_pk_fma_f32 v[114:115], s[58:59], v[28:29], v[114:115]
	v_exp_f32_e32 v109, v109
	v_pk_mul_f32 v[110:111], v[34:35], v[16:17] op_sel_hi:[0,1]
	v_pk_mul_f32 v[108:109], v[30:31], v[108:109]
	v_exp_f32_e32 v110, v110
	v_pk_fma_f32 v[30:31], v[112:113], s[44:45], v[108:109] op_sel_hi:[0,1,1]
	v_exp_f32_e32 v111, v111
	v_pk_fma_f32 v[114:115], s[60:61], v[30:31], v[114:115]
	v_pk_mul_f32 v[110:111], v[32:33], v[110:111]
	v_cvt_f32_f16_e32 v117, v46
	v_pk_fma_f32 v[32:33], v[112:113], s[46:47], v[110:111] op_sel_hi:[0,1,1]
	s_nop 0
	v_pk_fma_f32 v[114:115], s[62:63], v[32:33], v[114:115]
	s_nop 0
	v_add_f32_e32 v116, v114, v115
	v_fmac_f32_e32 v116, v98, v113
	v_mul_f32_e32 v116, v116, v117
	v_fma_mixlo_f16 v116, v116, s30, 0
	global_store_short v99, v116, s[26:27]
	s_add_u32 s26, s26, 0x1000
	s_addc_u32 s27, s27, 0
	s_waitcnt lgkmcnt(0)
	s_load_dwordx16 s[32:47], s[24:25], 0x100
	s_load_dwordx16 s[48:63], s[24:25], 0x140
	v_cvt_f32_f16_sdwa v113, v42 dst_sel:DWORD dst_unused:UNUSED_PAD src0_sel:WORD_1
	s_nop 0
	v_mul_f32_e32 v113, s29, v113
	v_mul_f32_e32 v112, v35, v113
	v_pk_mul_f32 v[104:105], v[34:35], v[2:3] op_sel:[1,0]
	v_pk_mul_f32 v[106:107], v[34:35], v[4:5] op_sel:[1,0]
	v_exp_f32_e32 v104, v104
	v_exp_f32_e32 v105, v105
	v_exp_f32_e32 v106, v106
	v_pk_mul_f32 v[104:105], v[18:19], v[104:105]
	v_exp_f32_e32 v107, v107
	v_pk_fma_f32 v[18:19], v[112:113], s[64:65], v[104:105] op_sel_hi:[0,1,1]
	v_pk_mul_f32 v[106:107], v[20:21], v[106:107]
	v_pk_fma_f32 v[114:115], s[80:81], v[18:19], 0 op_sel_hi:[1,1,0]
	v_pk_fma_f32 v[20:21], v[112:113], s[66:67], v[106:107] op_sel_hi:[0,1,1]
	v_pk_mul_f32 v[108:109], v[34:35], v[6:7] op_sel:[1,0]
	v_pk_fma_f32 v[114:115], s[82:83], v[20:21], v[114:115]
	v_exp_f32_e32 v108, v108
	v_exp_f32_e32 v109, v109
	v_pk_mul_f32 v[110:111], v[34:35], v[8:9] op_sel:[1,0]
	v_pk_mul_f32 v[108:109], v[22:23], v[108:109]
	v_exp_f32_e32 v110, v110
	v_pk_fma_f32 v[22:23], v[112:113], s[68:69], v[108:109] op_sel_hi:[0,1,1]
	v_exp_f32_e32 v111, v111
	v_pk_fma_f32 v[114:115], s[84:85], v[22:23], v[114:115]
	v_pk_mul_f32 v[110:111], v[24:25], v[110:111]
	v_pk_mul_f32 v[104:105], v[34:35], v[10:11] op_sel:[1,0]
	v_pk_fma_f32 v[24:25], v[112:113], s[70:71], v[110:111] op_sel_hi:[0,1,1]
	v_exp_f32_e32 v104, v104
	v_pk_fma_f32 v[114:115], s[86:87], v[24:25], v[114:115]
	v_exp_f32_e32 v105, v105
	v_pk_mul_f32 v[106:107], v[34:35], v[12:13] op_sel:[1,0]
	v_pk_mul_f32 v[104:105], v[26:27], v[104:105]
	v_exp_f32_e32 v106, v106
	v_pk_fma_f32 v[26:27], v[112:113], s[72:73], v[104:105] op_sel_hi:[0,1,1]
	v_exp_f32_e32 v107, v107
	v_pk_fma_f32 v[114:115], s[88:89], v[26:27], v[114:115]
	v_pk_mul_f32 v[106:107], v[28:29], v[106:107]
	v_pk_mul_f32 v[108:109], v[34:35], v[14:15] op_sel:[1,0]
	v_pk_fma_f32 v[28:29], v[112:113], s[74:75], v[106:107] op_sel_hi:[0,1,1]
	v_exp_f32_e32 v108, v108
	v_pk_fma_f32 v[114:115], s[90:91], v[28:29], v[114:115]
	v_exp_f32_e32 v109, v109
	v_pk_mul_f32 v[110:111], v[34:35], v[16:17] op_sel:[1,0]
	v_pk_mul_f32 v[108:109], v[30:31], v[108:109]
	v_exp_f32_e32 v110, v110
	v_pk_fma_f32 v[30:31], v[112:113], s[76:77], v[108:109] op_sel_hi:[0,1,1]
	v_exp_f32_e32 v111, v111
	v_pk_fma_f32 v[114:115], s[92:93], v[30:31], v[114:115]
	v_pk_mul_f32 v[110:111], v[32:33], v[110:111]
	v_cvt_f32_f16_sdwa v117, v46 dst_sel:DWORD dst_unused:UNUSED_PAD src0_sel:WORD_1
	v_pk_fma_f32 v[32:33], v[112:113], s[78:79], v[110:111] op_sel_hi:[0,1,1]
	s_nop 0
	v_pk_fma_f32 v[114:115], s[94:95], v[32:33], v[114:115]
	s_nop 0
	v_add_f32_e32 v116, v114, v115
	v_fmac_f32_e32 v116, v98, v113
	v_mul_f32_e32 v116, v116, v117
	v_fma_mixlo_f16 v116, v116, s30, 0
	global_store_short v99, v116, s[26:27]
	s_add_u32 s26, s26, 0x1000
	s_addc_u32 s27, s27, 0
	s_waitcnt lgkmcnt(0)
	s_load_dwordx16 s[64:79], s[24:25], 0x180
	s_load_dwordx16 s[80:95], s[24:25], 0x1c0
	v_cvt_f32_f16_e32 v113, v43
	v_mul_f32_e32 v113, s29, v113
	v_mul_f32_e32 v112, v36, v113
	v_pk_mul_f32 v[104:105], v[36:37], v[2:3] op_sel_hi:[0,1]
	v_pk_mul_f32 v[106:107], v[36:37], v[4:5] op_sel_hi:[0,1]
	v_exp_f32_e32 v104, v104
	v_exp_f32_e32 v105, v105
	v_exp_f32_e32 v106, v106
	v_pk_mul_f32 v[104:105], v[18:19], v[104:105]
	v_exp_f32_e32 v107, v107
	v_pk_fma_f32 v[18:19], v[112:113], s[32:33], v[104:105] op_sel_hi:[0,1,1]
	v_pk_mul_f32 v[106:107], v[20:21], v[106:107]
	v_pk_fma_f32 v[114:115], s[48:49], v[18:19], 0 op_sel_hi:[1,1,0]
	v_pk_fma_f32 v[20:21], v[112:113], s[34:35], v[106:107] op_sel_hi:[0,1,1]
	v_pk_mul_f32 v[108:109], v[36:37], v[6:7] op_sel_hi:[0,1]
	v_pk_fma_f32 v[114:115], s[50:51], v[20:21], v[114:115]
	v_exp_f32_e32 v108, v108
	v_exp_f32_e32 v109, v109
	v_pk_mul_f32 v[110:111], v[36:37], v[8:9] op_sel_hi:[0,1]
	v_pk_mul_f32 v[108:109], v[22:23], v[108:109]
	v_exp_f32_e32 v110, v110
	v_pk_fma_f32 v[22:23], v[112:113], s[36:37], v[108:109] op_sel_hi:[0,1,1]
	v_exp_f32_e32 v111, v111
	v_pk_fma_f32 v[114:115], s[52:53], v[22:23], v[114:115]
	v_pk_mul_f32 v[110:111], v[24:25], v[110:111]
	v_pk_mul_f32 v[104:105], v[36:37], v[10:11] op_sel_hi:[0,1]
	v_pk_fma_f32 v[24:25], v[112:113], s[38:39], v[110:111] op_sel_hi:[0,1,1]
	v_exp_f32_e32 v104, v104
	v_pk_fma_f32 v[114:115], s[54:55], v[24:25], v[114:115]
	v_exp_f32_e32 v105, v105
	v_pk_mul_f32 v[106:107], v[36:37], v[12:13] op_sel_hi:[0,1]
	v_pk_mul_f32 v[104:105], v[26:27], v[104:105]
	v_exp_f32_e32 v106, v106
	v_pk_fma_f32 v[26:27], v[112:113], s[40:41], v[104:105] op_sel_hi:[0,1,1]
	v_exp_f32_e32 v107, v107
	v_pk_fma_f32 v[114:115], s[56:57], v[26:27], v[114:115]
	v_pk_mul_f32 v[106:107], v[28:29], v[106:107]
	v_pk_mul_f32 v[108:109], v[36:37], v[14:15] op_sel_hi:[0,1]
	v_pk_fma_f32 v[28:29], v[112:113], s[42:43], v[106:107] op_sel_hi:[0,1,1]
	v_exp_f32_e32 v108, v108
	v_pk_fma_f32 v[114:115], s[58:59], v[28:29], v[114:115]
	v_exp_f32_e32 v109, v109
	v_pk_mul_f32 v[110:111], v[36:37], v[16:17] op_sel_hi:[0,1]
	v_pk_mul_f32 v[108:109], v[30:31], v[108:109]
	v_exp_f32_e32 v110, v110
	v_pk_fma_f32 v[30:31], v[112:113], s[44:45], v[108:109] op_sel_hi:[0,1,1]
	v_exp_f32_e32 v111, v111
	v_pk_fma_f32 v[114:115], s[60:61], v[30:31], v[114:115]
	v_pk_mul_f32 v[110:111], v[32:33], v[110:111]
	v_cvt_f32_f16_e32 v117, v47
	v_pk_fma_f32 v[32:33], v[112:113], s[46:47], v[110:111] op_sel_hi:[0,1,1]
	s_nop 0
	v_pk_fma_f32 v[114:115], s[62:63], v[32:33], v[114:115]
	s_nop 0
	v_add_f32_e32 v116, v114, v115
	v_fmac_f32_e32 v116, v98, v113
	v_mul_f32_e32 v116, v116, v117
	v_fma_mixlo_f16 v116, v116, s30, 0
	global_store_short v99, v116, s[26:27]
	s_add_u32 s26, s26, 0x1000
	s_addc_u32 s27, s27, 0
	s_waitcnt lgkmcnt(0)
	s_load_dwordx16 s[32:47], s[24:25], 0x200
	s_load_dwordx16 s[48:63], s[24:25], 0x240
	v_cvt_f32_f16_sdwa v113, v43 dst_sel:DWORD dst_unused:UNUSED_PAD src0_sel:WORD_1
	s_nop 0
	v_mul_f32_e32 v113, s29, v113
	v_mul_f32_e32 v112, v37, v113
	v_pk_mul_f32 v[104:105], v[36:37], v[2:3] op_sel:[1,0]
	v_pk_mul_f32 v[106:107], v[36:37], v[4:5] op_sel:[1,0]
	v_exp_f32_e32 v104, v104
	v_exp_f32_e32 v105, v105
	v_exp_f32_e32 v106, v106
	v_pk_mul_f32 v[104:105], v[18:19], v[104:105]
	v_exp_f32_e32 v107, v107
	v_pk_fma_f32 v[18:19], v[112:113], s[64:65], v[104:105] op_sel_hi:[0,1,1]
	v_pk_mul_f32 v[106:107], v[20:21], v[106:107]
	v_pk_fma_f32 v[114:115], s[80:81], v[18:19], 0 op_sel_hi:[1,1,0]
	v_pk_fma_f32 v[20:21], v[112:113], s[66:67], v[106:107] op_sel_hi:[0,1,1]
	v_pk_mul_f32 v[108:109], v[36:37], v[6:7] op_sel:[1,0]
	v_pk_fma_f32 v[114:115], s[82:83], v[20:21], v[114:115]
	v_exp_f32_e32 v108, v108
	v_exp_f32_e32 v109, v109
	v_pk_mul_f32 v[110:111], v[36:37], v[8:9] op_sel:[1,0]
	v_pk_mul_f32 v[108:109], v[22:23], v[108:109]
	v_exp_f32_e32 v110, v110
	v_pk_fma_f32 v[22:23], v[112:113], s[68:69], v[108:109] op_sel_hi:[0,1,1]
	v_exp_f32_e32 v111, v111
	v_pk_fma_f32 v[114:115], s[84:85], v[22:23], v[114:115]
	v_pk_mul_f32 v[110:111], v[24:25], v[110:111]
	v_pk_mul_f32 v[104:105], v[36:37], v[10:11] op_sel:[1,0]
	v_pk_fma_f32 v[24:25], v[112:113], s[70:71], v[110:111] op_sel_hi:[0,1,1]
	v_exp_f32_e32 v104, v104
	v_pk_fma_f32 v[114:115], s[86:87], v[24:25], v[114:115]
	v_exp_f32_e32 v105, v105
	v_pk_mul_f32 v[106:107], v[36:37], v[12:13] op_sel:[1,0]
	v_pk_mul_f32 v[104:105], v[26:27], v[104:105]
	v_exp_f32_e32 v106, v106
	v_pk_fma_f32 v[26:27], v[112:113], s[72:73], v[104:105] op_sel_hi:[0,1,1]
	v_exp_f32_e32 v107, v107
	v_pk_fma_f32 v[114:115], s[88:89], v[26:27], v[114:115]
	v_pk_mul_f32 v[106:107], v[28:29], v[106:107]
	v_pk_mul_f32 v[108:109], v[36:37], v[14:15] op_sel:[1,0]
	v_pk_fma_f32 v[28:29], v[112:113], s[74:75], v[106:107] op_sel_hi:[0,1,1]
	v_exp_f32_e32 v108, v108
	v_pk_fma_f32 v[114:115], s[90:91], v[28:29], v[114:115]
	v_exp_f32_e32 v109, v109
	v_pk_mul_f32 v[110:111], v[36:37], v[16:17] op_sel:[1,0]
	v_pk_mul_f32 v[108:109], v[30:31], v[108:109]
	v_exp_f32_e32 v110, v110
	v_pk_fma_f32 v[30:31], v[112:113], s[76:77], v[108:109] op_sel_hi:[0,1,1]
	v_exp_f32_e32 v111, v111
	v_pk_fma_f32 v[114:115], s[92:93], v[30:31], v[114:115]
	v_pk_mul_f32 v[110:111], v[32:33], v[110:111]
	v_cvt_f32_f16_sdwa v117, v47 dst_sel:DWORD dst_unused:UNUSED_PAD src0_sel:WORD_1
	v_pk_fma_f32 v[32:33], v[112:113], s[78:79], v[110:111] op_sel_hi:[0,1,1]
	s_nop 0
	v_pk_fma_f32 v[114:115], s[94:95], v[32:33], v[114:115]
	s_nop 0
	v_add_f32_e32 v116, v114, v115
	v_fmac_f32_e32 v116, v98, v113
	v_mul_f32_e32 v116, v116, v117
	v_fma_mixlo_f16 v116, v116, s30, 0
	global_store_short v99, v116, s[26:27]
	s_add_u32 s26, s26, 0x1000
	s_addc_u32 s27, s27, 0
	s_waitcnt lgkmcnt(0)
	s_load_dwordx16 s[64:79], s[24:25], 0x280
	s_load_dwordx16 s[80:95], s[24:25], 0x2c0
	v_cvt_f32_f16_e32 v113, v44
	v_mul_f32_e32 v113, s29, v113
	v_mul_f32_e32 v112, v38, v113
	v_pk_mul_f32 v[104:105], v[38:39], v[2:3] op_sel_hi:[0,1]
	v_pk_mul_f32 v[106:107], v[38:39], v[4:5] op_sel_hi:[0,1]
	v_exp_f32_e32 v104, v104
	v_exp_f32_e32 v105, v105
	v_exp_f32_e32 v106, v106
	v_pk_mul_f32 v[104:105], v[18:19], v[104:105]
	v_exp_f32_e32 v107, v107
	v_pk_fma_f32 v[18:19], v[112:113], s[32:33], v[104:105] op_sel_hi:[0,1,1]
	v_pk_mul_f32 v[106:107], v[20:21], v[106:107]
	v_pk_fma_f32 v[114:115], s[48:49], v[18:19], 0 op_sel_hi:[1,1,0]
	v_pk_fma_f32 v[20:21], v[112:113], s[34:35], v[106:107] op_sel_hi:[0,1,1]
	v_pk_mul_f32 v[108:109], v[38:39], v[6:7] op_sel_hi:[0,1]
	v_pk_fma_f32 v[114:115], s[50:51], v[20:21], v[114:115]
	v_exp_f32_e32 v108, v108
	v_exp_f32_e32 v109, v109
	v_pk_mul_f32 v[110:111], v[38:39], v[8:9] op_sel_hi:[0,1]
	v_pk_mul_f32 v[108:109], v[22:23], v[108:109]
	v_exp_f32_e32 v110, v110
	v_pk_fma_f32 v[22:23], v[112:113], s[36:37], v[108:109] op_sel_hi:[0,1,1]
	v_exp_f32_e32 v111, v111
	v_pk_fma_f32 v[114:115], s[52:53], v[22:23], v[114:115]
	v_pk_mul_f32 v[110:111], v[24:25], v[110:111]
	v_pk_mul_f32 v[104:105], v[38:39], v[10:11] op_sel_hi:[0,1]
	v_pk_fma_f32 v[24:25], v[112:113], s[38:39], v[110:111] op_sel_hi:[0,1,1]
	v_exp_f32_e32 v104, v104
	v_pk_fma_f32 v[114:115], s[54:55], v[24:25], v[114:115]
	v_exp_f32_e32 v105, v105
	v_pk_mul_f32 v[106:107], v[38:39], v[12:13] op_sel_hi:[0,1]
	v_pk_mul_f32 v[104:105], v[26:27], v[104:105]
	v_exp_f32_e32 v106, v106
	v_pk_fma_f32 v[26:27], v[112:113], s[40:41], v[104:105] op_sel_hi:[0,1,1]
	v_exp_f32_e32 v107, v107
	v_pk_fma_f32 v[114:115], s[56:57], v[26:27], v[114:115]
	v_pk_mul_f32 v[106:107], v[28:29], v[106:107]
	v_pk_mul_f32 v[108:109], v[38:39], v[14:15] op_sel_hi:[0,1]
	v_pk_fma_f32 v[28:29], v[112:113], s[42:43], v[106:107] op_sel_hi:[0,1,1]
	v_exp_f32_e32 v108, v108
	v_pk_fma_f32 v[114:115], s[58:59], v[28:29], v[114:115]
	v_exp_f32_e32 v109, v109
	v_pk_mul_f32 v[110:111], v[38:39], v[16:17] op_sel_hi:[0,1]
	v_pk_mul_f32 v[108:109], v[30:31], v[108:109]
	v_exp_f32_e32 v110, v110
	v_pk_fma_f32 v[30:31], v[112:113], s[44:45], v[108:109] op_sel_hi:[0,1,1]
	v_exp_f32_e32 v111, v111
	v_pk_fma_f32 v[114:115], s[60:61], v[30:31], v[114:115]
	v_pk_mul_f32 v[110:111], v[32:33], v[110:111]
	v_cvt_f32_f16_e32 v117, v48
	v_pk_fma_f32 v[32:33], v[112:113], s[46:47], v[110:111] op_sel_hi:[0,1,1]
	s_nop 0
	v_pk_fma_f32 v[114:115], s[62:63], v[32:33], v[114:115]
	s_nop 0
	v_add_f32_e32 v116, v114, v115
	v_fmac_f32_e32 v116, v98, v113
	v_mul_f32_e32 v116, v116, v117
	v_fma_mixlo_f16 v116, v116, s30, 0
	global_store_short v99, v116, s[26:27]
	s_add_u32 s26, s26, 0x1000
	s_addc_u32 s27, s27, 0
	s_waitcnt lgkmcnt(0)
	s_load_dwordx16 s[32:47], s[24:25], 0x300
	s_load_dwordx16 s[48:63], s[24:25], 0x340
	v_cvt_f32_f16_sdwa v113, v44 dst_sel:DWORD dst_unused:UNUSED_PAD src0_sel:WORD_1
	s_nop 0
	v_mul_f32_e32 v113, s29, v113
	v_mul_f32_e32 v112, v39, v113
	v_pk_mul_f32 v[104:105], v[38:39], v[2:3] op_sel:[1,0]
	v_pk_mul_f32 v[106:107], v[38:39], v[4:5] op_sel:[1,0]
	v_exp_f32_e32 v104, v104
	v_exp_f32_e32 v105, v105
	v_exp_f32_e32 v106, v106
	v_pk_mul_f32 v[104:105], v[18:19], v[104:105]
	v_exp_f32_e32 v107, v107
	v_pk_fma_f32 v[18:19], v[112:113], s[64:65], v[104:105] op_sel_hi:[0,1,1]
	v_pk_mul_f32 v[106:107], v[20:21], v[106:107]
	v_pk_fma_f32 v[114:115], s[80:81], v[18:19], 0 op_sel_hi:[1,1,0]
	v_pk_fma_f32 v[20:21], v[112:113], s[66:67], v[106:107] op_sel_hi:[0,1,1]
	v_pk_mul_f32 v[108:109], v[38:39], v[6:7] op_sel:[1,0]
	v_pk_fma_f32 v[114:115], s[82:83], v[20:21], v[114:115]
	v_exp_f32_e32 v108, v108
	v_exp_f32_e32 v109, v109
	v_pk_mul_f32 v[110:111], v[38:39], v[8:9] op_sel:[1,0]
	v_pk_mul_f32 v[108:109], v[22:23], v[108:109]
	v_exp_f32_e32 v110, v110
	v_pk_fma_f32 v[22:23], v[112:113], s[68:69], v[108:109] op_sel_hi:[0,1,1]
	v_exp_f32_e32 v111, v111
	v_pk_fma_f32 v[114:115], s[84:85], v[22:23], v[114:115]
	v_pk_mul_f32 v[110:111], v[24:25], v[110:111]
	v_pk_mul_f32 v[104:105], v[38:39], v[10:11] op_sel:[1,0]
	v_pk_fma_f32 v[24:25], v[112:113], s[70:71], v[110:111] op_sel_hi:[0,1,1]
	v_exp_f32_e32 v104, v104
	v_pk_fma_f32 v[114:115], s[86:87], v[24:25], v[114:115]
	v_exp_f32_e32 v105, v105
	v_pk_mul_f32 v[106:107], v[38:39], v[12:13] op_sel:[1,0]
	v_pk_mul_f32 v[104:105], v[26:27], v[104:105]
	v_exp_f32_e32 v106, v106
	v_pk_fma_f32 v[26:27], v[112:113], s[72:73], v[104:105] op_sel_hi:[0,1,1]
	v_exp_f32_e32 v107, v107
	v_pk_fma_f32 v[114:115], s[88:89], v[26:27], v[114:115]
	v_pk_mul_f32 v[106:107], v[28:29], v[106:107]
	v_pk_mul_f32 v[108:109], v[38:39], v[14:15] op_sel:[1,0]
	v_pk_fma_f32 v[28:29], v[112:113], s[74:75], v[106:107] op_sel_hi:[0,1,1]
	v_exp_f32_e32 v108, v108
	v_pk_fma_f32 v[114:115], s[90:91], v[28:29], v[114:115]
	v_exp_f32_e32 v109, v109
	v_pk_mul_f32 v[110:111], v[38:39], v[16:17] op_sel:[1,0]
	v_pk_mul_f32 v[108:109], v[30:31], v[108:109]
	v_exp_f32_e32 v110, v110
	v_pk_fma_f32 v[30:31], v[112:113], s[76:77], v[108:109] op_sel_hi:[0,1,1]
	v_exp_f32_e32 v111, v111
	v_pk_fma_f32 v[114:115], s[92:93], v[30:31], v[114:115]
	v_pk_mul_f32 v[110:111], v[32:33], v[110:111]
	v_cvt_f32_f16_sdwa v117, v48 dst_sel:DWORD dst_unused:UNUSED_PAD src0_sel:WORD_1
	v_pk_fma_f32 v[32:33], v[112:113], s[78:79], v[110:111] op_sel_hi:[0,1,1]
	s_nop 0
	v_pk_fma_f32 v[114:115], s[94:95], v[32:33], v[114:115]
	s_nop 0
	v_add_f32_e32 v116, v114, v115
	v_fmac_f32_e32 v116, v98, v113
	v_mul_f32_e32 v116, v116, v117
	v_fma_mixlo_f16 v116, v116, s30, 0
	global_store_short v99, v116, s[26:27]
	s_add_u32 s26, s26, 0x1000
	s_addc_u32 s27, s27, 0
	s_waitcnt lgkmcnt(0)
	s_load_dwordx16 s[64:79], s[24:25], 0x380
	s_load_dwordx16 s[80:95], s[24:25], 0x3c0
	v_cvt_f32_f16_e32 v113, v45
	v_mul_f32_e32 v113, s29, v113
	v_mul_f32_e32 v112, v40, v113
	v_pk_mul_f32 v[104:105], v[40:41], v[2:3] op_sel_hi:[0,1]
	v_pk_mul_f32 v[106:107], v[40:41], v[4:5] op_sel_hi:[0,1]
	v_exp_f32_e32 v104, v104
	v_exp_f32_e32 v105, v105
	v_exp_f32_e32 v106, v106
	v_pk_mul_f32 v[104:105], v[18:19], v[104:105]
	v_exp_f32_e32 v107, v107
	v_pk_fma_f32 v[18:19], v[112:113], s[32:33], v[104:105] op_sel_hi:[0,1,1]
	v_pk_mul_f32 v[106:107], v[20:21], v[106:107]
	v_pk_fma_f32 v[114:115], s[48:49], v[18:19], 0 op_sel_hi:[1,1,0]
	v_pk_fma_f32 v[20:21], v[112:113], s[34:35], v[106:107] op_sel_hi:[0,1,1]
	v_pk_mul_f32 v[108:109], v[40:41], v[6:7] op_sel_hi:[0,1]
	v_pk_fma_f32 v[114:115], s[50:51], v[20:21], v[114:115]
	v_exp_f32_e32 v108, v108
	v_exp_f32_e32 v109, v109
	v_pk_mul_f32 v[110:111], v[40:41], v[8:9] op_sel_hi:[0,1]
	v_pk_mul_f32 v[108:109], v[22:23], v[108:109]
	v_exp_f32_e32 v110, v110
	v_pk_fma_f32 v[22:23], v[112:113], s[36:37], v[108:109] op_sel_hi:[0,1,1]
	v_exp_f32_e32 v111, v111
	v_pk_fma_f32 v[114:115], s[52:53], v[22:23], v[114:115]
	v_pk_mul_f32 v[110:111], v[24:25], v[110:111]
	v_pk_mul_f32 v[104:105], v[40:41], v[10:11] op_sel_hi:[0,1]
	v_pk_fma_f32 v[24:25], v[112:113], s[38:39], v[110:111] op_sel_hi:[0,1,1]
	v_exp_f32_e32 v104, v104
	v_pk_fma_f32 v[114:115], s[54:55], v[24:25], v[114:115]
	v_exp_f32_e32 v105, v105
	v_pk_mul_f32 v[106:107], v[40:41], v[12:13] op_sel_hi:[0,1]
	v_pk_mul_f32 v[104:105], v[26:27], v[104:105]
	v_exp_f32_e32 v106, v106
	v_pk_fma_f32 v[26:27], v[112:113], s[40:41], v[104:105] op_sel_hi:[0,1,1]
	v_exp_f32_e32 v107, v107
	v_pk_fma_f32 v[114:115], s[56:57], v[26:27], v[114:115]
	v_pk_mul_f32 v[106:107], v[28:29], v[106:107]
	v_pk_mul_f32 v[108:109], v[40:41], v[14:15] op_sel_hi:[0,1]
	v_pk_fma_f32 v[28:29], v[112:113], s[42:43], v[106:107] op_sel_hi:[0,1,1]
	v_exp_f32_e32 v108, v108
	v_pk_fma_f32 v[114:115], s[58:59], v[28:29], v[114:115]
	v_exp_f32_e32 v109, v109
	v_pk_mul_f32 v[110:111], v[40:41], v[16:17] op_sel_hi:[0,1]
	v_pk_mul_f32 v[108:109], v[30:31], v[108:109]
	v_exp_f32_e32 v110, v110
	v_pk_fma_f32 v[30:31], v[112:113], s[44:45], v[108:109] op_sel_hi:[0,1,1]
	v_exp_f32_e32 v111, v111
	v_pk_fma_f32 v[114:115], s[60:61], v[30:31], v[114:115]
	v_pk_mul_f32 v[110:111], v[32:33], v[110:111]
	v_cvt_f32_f16_e32 v117, v49
	v_pk_fma_f32 v[32:33], v[112:113], s[46:47], v[110:111] op_sel_hi:[0,1,1]
	s_nop 0
	v_pk_fma_f32 v[114:115], s[62:63], v[32:33], v[114:115]
	s_nop 0
	v_add_f32_e32 v116, v114, v115
	v_fmac_f32_e32 v116, v98, v113
	v_mul_f32_e32 v116, v116, v117
	v_fma_mixlo_f16 v116, v116, s30, 0
	global_store_short v99, v116, s[26:27]
	s_add_u32 s26, s26, 0x1000
	s_addc_u32 s27, s27, 0
	s_waitcnt lgkmcnt(0)
	s_load_dwordx16 s[32:47], s[24:25], 0x400
	s_load_dwordx16 s[48:63], s[24:25], 0x440
	v_cvt_f32_f16_sdwa v113, v45 dst_sel:DWORD dst_unused:UNUSED_PAD src0_sel:WORD_1
	s_nop 0
	v_mul_f32_e32 v113, s29, v113
	v_mul_f32_e32 v112, v41, v113
	v_pk_mul_f32 v[104:105], v[40:41], v[2:3] op_sel:[1,0]
	v_pk_mul_f32 v[106:107], v[40:41], v[4:5] op_sel:[1,0]
	v_exp_f32_e32 v104, v104
	v_exp_f32_e32 v105, v105
	v_exp_f32_e32 v106, v106
	v_pk_mul_f32 v[104:105], v[18:19], v[104:105]
	v_exp_f32_e32 v107, v107
	v_pk_fma_f32 v[18:19], v[112:113], s[64:65], v[104:105] op_sel_hi:[0,1,1]
	v_pk_mul_f32 v[106:107], v[20:21], v[106:107]
	v_pk_fma_f32 v[114:115], s[80:81], v[18:19], 0 op_sel_hi:[1,1,0]
	v_pk_fma_f32 v[20:21], v[112:113], s[66:67], v[106:107] op_sel_hi:[0,1,1]
	v_pk_mul_f32 v[108:109], v[40:41], v[6:7] op_sel:[1,0]
	v_pk_fma_f32 v[114:115], s[82:83], v[20:21], v[114:115]
	v_exp_f32_e32 v108, v108
	v_exp_f32_e32 v109, v109
	v_pk_mul_f32 v[110:111], v[40:41], v[8:9] op_sel:[1,0]
	v_pk_mul_f32 v[108:109], v[22:23], v[108:109]
	v_exp_f32_e32 v110, v110
	v_pk_fma_f32 v[22:23], v[112:113], s[68:69], v[108:109] op_sel_hi:[0,1,1]
	v_exp_f32_e32 v111, v111
	v_pk_fma_f32 v[114:115], s[84:85], v[22:23], v[114:115]
	v_pk_mul_f32 v[110:111], v[24:25], v[110:111]
	v_pk_mul_f32 v[104:105], v[40:41], v[10:11] op_sel:[1,0]
	v_pk_fma_f32 v[24:25], v[112:113], s[70:71], v[110:111] op_sel_hi:[0,1,1]
	v_exp_f32_e32 v104, v104
	v_pk_fma_f32 v[114:115], s[86:87], v[24:25], v[114:115]
	v_exp_f32_e32 v105, v105
	v_pk_mul_f32 v[106:107], v[40:41], v[12:13] op_sel:[1,0]
	v_pk_mul_f32 v[104:105], v[26:27], v[104:105]
	v_exp_f32_e32 v106, v106
	v_pk_fma_f32 v[26:27], v[112:113], s[72:73], v[104:105] op_sel_hi:[0,1,1]
	v_exp_f32_e32 v107, v107
	v_pk_fma_f32 v[114:115], s[88:89], v[26:27], v[114:115]
	v_pk_mul_f32 v[106:107], v[28:29], v[106:107]
	v_pk_mul_f32 v[108:109], v[40:41], v[14:15] op_sel:[1,0]
	v_pk_fma_f32 v[28:29], v[112:113], s[74:75], v[106:107] op_sel_hi:[0,1,1]
	v_exp_f32_e32 v108, v108
	v_pk_fma_f32 v[114:115], s[90:91], v[28:29], v[114:115]
	v_exp_f32_e32 v109, v109
	v_pk_mul_f32 v[110:111], v[40:41], v[16:17] op_sel:[1,0]
	v_pk_mul_f32 v[108:109], v[30:31], v[108:109]
	v_exp_f32_e32 v110, v110
	v_pk_fma_f32 v[30:31], v[112:113], s[76:77], v[108:109] op_sel_hi:[0,1,1]
	v_exp_f32_e32 v111, v111
	v_pk_fma_f32 v[114:115], s[92:93], v[30:31], v[114:115]
	v_pk_mul_f32 v[110:111], v[32:33], v[110:111]
	v_cvt_f32_f16_sdwa v117, v49 dst_sel:DWORD dst_unused:UNUSED_PAD src0_sel:WORD_1
	v_pk_fma_f32 v[32:33], v[112:113], s[78:79], v[110:111] op_sel_hi:[0,1,1]
	s_nop 0
	v_pk_fma_f32 v[114:115], s[94:95], v[32:33], v[114:115]
	s_nop 0
	v_add_f32_e32 v116, v114, v115
	v_fmac_f32_e32 v116, v98, v113
	v_mul_f32_e32 v116, v116, v117
	v_fma_mixlo_f16 v116, v116, s30, 0
	global_store_short v99, v116, s[26:27]
	s_add_u32 s26, s26, 0x1000
	s_addc_u32 s27, s27, 0
	s_waitcnt vmcnt(13)
	global_load_dwordx4 v[82:85], v102, s[0:1]
	s_add_u32 s0, s0, 0x8000
	s_addc_u32 s1, s1, 0
	global_load_dwordx4 v[90:93], v102, s[8:9]
	s_add_u32 s8, s8, 0x8000
	s_addc_u32 s9, s9, 0
	global_load_dwordx2 v[94:95], v103, s[2:3]
	s_add_u32 s2, s2, 0x8000
	s_addc_u32 s3, s3, 0
	global_load_dwordx4 v[86:89], v102, s[0:1]
	s_add_u32 s0, s0, 0x8000
	s_addc_u32 s1, s1, 0
	global_load_dwordx2 v[96:97], v103, s[2:3]
	s_add_u32 s2, s2, 0x8000
	s_addc_u32 s3, s3, 0
	s_waitcnt lgkmcnt(0)
	s_load_dwordx16 s[64:79], s[24:25], 0x480
	s_load_dwordx16 s[80:95], s[24:25], 0x4c0
	v_cvt_f32_f16_e32 v113, v58
	v_mul_f32_e32 v113, s29, v113
	v_mul_f32_e32 v112, v50, v113
	v_pk_mul_f32 v[104:105], v[50:51], v[2:3] op_sel_hi:[0,1]
	v_pk_mul_f32 v[106:107], v[50:51], v[4:5] op_sel_hi:[0,1]
	v_exp_f32_e32 v104, v104
	v_exp_f32_e32 v105, v105
	v_exp_f32_e32 v106, v106
	v_pk_mul_f32 v[104:105], v[18:19], v[104:105]
	v_exp_f32_e32 v107, v107
	v_pk_fma_f32 v[18:19], v[112:113], s[32:33], v[104:105] op_sel_hi:[0,1,1]
	v_pk_mul_f32 v[106:107], v[20:21], v[106:107]
	v_pk_fma_f32 v[114:115], s[48:49], v[18:19], 0 op_sel_hi:[1,1,0]
	v_pk_fma_f32 v[20:21], v[112:113], s[34:35], v[106:107] op_sel_hi:[0,1,1]
	v_pk_mul_f32 v[108:109], v[50:51], v[6:7] op_sel_hi:[0,1]
	v_pk_fma_f32 v[114:115], s[50:51], v[20:21], v[114:115]
	v_exp_f32_e32 v108, v108
	v_exp_f32_e32 v109, v109
	v_pk_mul_f32 v[110:111], v[50:51], v[8:9] op_sel_hi:[0,1]
	v_pk_mul_f32 v[108:109], v[22:23], v[108:109]
	v_exp_f32_e32 v110, v110
	v_pk_fma_f32 v[22:23], v[112:113], s[36:37], v[108:109] op_sel_hi:[0,1,1]
	v_exp_f32_e32 v111, v111
	v_pk_fma_f32 v[114:115], s[52:53], v[22:23], v[114:115]
	v_pk_mul_f32 v[110:111], v[24:25], v[110:111]
	v_pk_mul_f32 v[104:105], v[50:51], v[10:11] op_sel_hi:[0,1]
	v_pk_fma_f32 v[24:25], v[112:113], s[38:39], v[110:111] op_sel_hi:[0,1,1]
	v_exp_f32_e32 v104, v104
	v_pk_fma_f32 v[114:115], s[54:55], v[24:25], v[114:115]
	v_exp_f32_e32 v105, v105
	v_pk_mul_f32 v[106:107], v[50:51], v[12:13] op_sel_hi:[0,1]
	v_pk_mul_f32 v[104:105], v[26:27], v[104:105]
	v_exp_f32_e32 v106, v106
	v_pk_fma_f32 v[26:27], v[112:113], s[40:41], v[104:105] op_sel_hi:[0,1,1]
	v_exp_f32_e32 v107, v107
	v_pk_fma_f32 v[114:115], s[56:57], v[26:27], v[114:115]
	v_pk_mul_f32 v[106:107], v[28:29], v[106:107]
	v_pk_mul_f32 v[108:109], v[50:51], v[14:15] op_sel_hi:[0,1]
	v_pk_fma_f32 v[28:29], v[112:113], s[42:43], v[106:107] op_sel_hi:[0,1,1]
	v_exp_f32_e32 v108, v108
	v_pk_fma_f32 v[114:115], s[58:59], v[28:29], v[114:115]
	v_exp_f32_e32 v109, v109
	v_pk_mul_f32 v[110:111], v[50:51], v[16:17] op_sel_hi:[0,1]
	v_pk_mul_f32 v[108:109], v[30:31], v[108:109]
	v_exp_f32_e32 v110, v110
	v_pk_fma_f32 v[30:31], v[112:113], s[44:45], v[108:109] op_sel_hi:[0,1,1]
	v_exp_f32_e32 v111, v111
	v_pk_fma_f32 v[114:115], s[60:61], v[30:31], v[114:115]
	v_pk_mul_f32 v[110:111], v[32:33], v[110:111]
	v_cvt_f32_f16_e32 v117, v62
	v_pk_fma_f32 v[32:33], v[112:113], s[46:47], v[110:111] op_sel_hi:[0,1,1]
	s_nop 0
	v_pk_fma_f32 v[114:115], s[62:63], v[32:33], v[114:115]
	s_nop 0
	v_add_f32_e32 v116, v114, v115
	v_fmac_f32_e32 v116, v98, v113
	v_mul_f32_e32 v116, v116, v117
	v_fma_mixlo_f16 v116, v116, s30, 0
	global_store_short v99, v116, s[26:27]
	s_add_u32 s26, s26, 0x1000
	s_addc_u32 s27, s27, 0
	s_waitcnt lgkmcnt(0)
	s_load_dwordx16 s[32:47], s[24:25], 0x500
	s_load_dwordx16 s[48:63], s[24:25], 0x540
	v_cvt_f32_f16_sdwa v113, v58 dst_sel:DWORD dst_unused:UNUSED_PAD src0_sel:WORD_1
	s_nop 0
	v_mul_f32_e32 v113, s29, v113
	v_mul_f32_e32 v112, v51, v113
	v_pk_mul_f32 v[104:105], v[50:51], v[2:3] op_sel:[1,0]
	v_pk_mul_f32 v[106:107], v[50:51], v[4:5] op_sel:[1,0]
	v_exp_f32_e32 v104, v104
	v_exp_f32_e32 v105, v105
	v_exp_f32_e32 v106, v106
	v_pk_mul_f32 v[104:105], v[18:19], v[104:105]
	v_exp_f32_e32 v107, v107
	v_pk_fma_f32 v[18:19], v[112:113], s[64:65], v[104:105] op_sel_hi:[0,1,1]
	v_pk_mul_f32 v[106:107], v[20:21], v[106:107]
	v_pk_fma_f32 v[114:115], s[80:81], v[18:19], 0 op_sel_hi:[1,1,0]
	v_pk_fma_f32 v[20:21], v[112:113], s[66:67], v[106:107] op_sel_hi:[0,1,1]
	v_pk_mul_f32 v[108:109], v[50:51], v[6:7] op_sel:[1,0]
	v_pk_fma_f32 v[114:115], s[82:83], v[20:21], v[114:115]
	v_exp_f32_e32 v108, v108
	v_exp_f32_e32 v109, v109
	v_pk_mul_f32 v[110:111], v[50:51], v[8:9] op_sel:[1,0]
	v_pk_mul_f32 v[108:109], v[22:23], v[108:109]
	v_exp_f32_e32 v110, v110
	v_pk_fma_f32 v[22:23], v[112:113], s[68:69], v[108:109] op_sel_hi:[0,1,1]
	v_exp_f32_e32 v111, v111
	v_pk_fma_f32 v[114:115], s[84:85], v[22:23], v[114:115]
	v_pk_mul_f32 v[110:111], v[24:25], v[110:111]
	v_pk_mul_f32 v[104:105], v[50:51], v[10:11] op_sel:[1,0]
	v_pk_fma_f32 v[24:25], v[112:113], s[70:71], v[110:111] op_sel_hi:[0,1,1]
	v_exp_f32_e32 v104, v104
	v_pk_fma_f32 v[114:115], s[86:87], v[24:25], v[114:115]
	v_exp_f32_e32 v105, v105
	v_pk_mul_f32 v[106:107], v[50:51], v[12:13] op_sel:[1,0]
	v_pk_mul_f32 v[104:105], v[26:27], v[104:105]
	v_exp_f32_e32 v106, v106
	v_pk_fma_f32 v[26:27], v[112:113], s[72:73], v[104:105] op_sel_hi:[0,1,1]
	v_exp_f32_e32 v107, v107
	v_pk_fma_f32 v[114:115], s[88:89], v[26:27], v[114:115]
	v_pk_mul_f32 v[106:107], v[28:29], v[106:107]
	v_pk_mul_f32 v[108:109], v[50:51], v[14:15] op_sel:[1,0]
	v_pk_fma_f32 v[28:29], v[112:113], s[74:75], v[106:107] op_sel_hi:[0,1,1]
	v_exp_f32_e32 v108, v108
	v_pk_fma_f32 v[114:115], s[90:91], v[28:29], v[114:115]
	v_exp_f32_e32 v109, v109
	v_pk_mul_f32 v[110:111], v[50:51], v[16:17] op_sel:[1,0]
	v_pk_mul_f32 v[108:109], v[30:31], v[108:109]
	v_exp_f32_e32 v110, v110
	v_pk_fma_f32 v[30:31], v[112:113], s[76:77], v[108:109] op_sel_hi:[0,1,1]
	v_exp_f32_e32 v111, v111
	v_pk_fma_f32 v[114:115], s[92:93], v[30:31], v[114:115]
	v_pk_mul_f32 v[110:111], v[32:33], v[110:111]
	v_cvt_f32_f16_sdwa v117, v62 dst_sel:DWORD dst_unused:UNUSED_PAD src0_sel:WORD_1
	v_pk_fma_f32 v[32:33], v[112:113], s[78:79], v[110:111] op_sel_hi:[0,1,1]
	s_nop 0
	v_pk_fma_f32 v[114:115], s[94:95], v[32:33], v[114:115]
	s_nop 0
	v_add_f32_e32 v116, v114, v115
	v_fmac_f32_e32 v116, v98, v113
	v_mul_f32_e32 v116, v116, v117
	v_fma_mixlo_f16 v116, v116, s30, 0
	global_store_short v99, v116, s[26:27]
	s_add_u32 s26, s26, 0x1000
	s_addc_u32 s27, s27, 0
	s_waitcnt lgkmcnt(0)
	s_load_dwordx16 s[64:79], s[24:25], 0x580
	s_load_dwordx16 s[80:95], s[24:25], 0x5c0
	v_cvt_f32_f16_e32 v113, v59
	v_mul_f32_e32 v113, s29, v113
	v_mul_f32_e32 v112, v52, v113
	v_pk_mul_f32 v[104:105], v[52:53], v[2:3] op_sel_hi:[0,1]
	v_pk_mul_f32 v[106:107], v[52:53], v[4:5] op_sel_hi:[0,1]
	v_exp_f32_e32 v104, v104
	v_exp_f32_e32 v105, v105
	v_exp_f32_e32 v106, v106
	v_pk_mul_f32 v[104:105], v[18:19], v[104:105]
	v_exp_f32_e32 v107, v107
	v_pk_fma_f32 v[18:19], v[112:113], s[32:33], v[104:105] op_sel_hi:[0,1,1]
	v_pk_mul_f32 v[106:107], v[20:21], v[106:107]
	v_pk_fma_f32 v[114:115], s[48:49], v[18:19], 0 op_sel_hi:[1,1,0]
	v_pk_fma_f32 v[20:21], v[112:113], s[34:35], v[106:107] op_sel_hi:[0,1,1]
	v_pk_mul_f32 v[108:109], v[52:53], v[6:7] op_sel_hi:[0,1]
	v_pk_fma_f32 v[114:115], s[50:51], v[20:21], v[114:115]
	v_exp_f32_e32 v108, v108
	v_exp_f32_e32 v109, v109
	v_pk_mul_f32 v[110:111], v[52:53], v[8:9] op_sel_hi:[0,1]
	v_pk_mul_f32 v[108:109], v[22:23], v[108:109]
	v_exp_f32_e32 v110, v110
	v_pk_fma_f32 v[22:23], v[112:113], s[36:37], v[108:109] op_sel_hi:[0,1,1]
	v_exp_f32_e32 v111, v111
	v_pk_fma_f32 v[114:115], s[52:53], v[22:23], v[114:115]
	v_pk_mul_f32 v[110:111], v[24:25], v[110:111]
	v_pk_mul_f32 v[104:105], v[52:53], v[10:11] op_sel_hi:[0,1]
	v_pk_fma_f32 v[24:25], v[112:113], s[38:39], v[110:111] op_sel_hi:[0,1,1]
	v_exp_f32_e32 v104, v104
	v_pk_fma_f32 v[114:115], s[54:55], v[24:25], v[114:115]
	v_exp_f32_e32 v105, v105
	v_pk_mul_f32 v[106:107], v[52:53], v[12:13] op_sel_hi:[0,1]
	v_pk_mul_f32 v[104:105], v[26:27], v[104:105]
	v_exp_f32_e32 v106, v106
	v_pk_fma_f32 v[26:27], v[112:113], s[40:41], v[104:105] op_sel_hi:[0,1,1]
	v_exp_f32_e32 v107, v107
	v_pk_fma_f32 v[114:115], s[56:57], v[26:27], v[114:115]
	v_pk_mul_f32 v[106:107], v[28:29], v[106:107]
	v_pk_mul_f32 v[108:109], v[52:53], v[14:15] op_sel_hi:[0,1]
	v_pk_fma_f32 v[28:29], v[112:113], s[42:43], v[106:107] op_sel_hi:[0,1,1]
	v_exp_f32_e32 v108, v108
	v_pk_fma_f32 v[114:115], s[58:59], v[28:29], v[114:115]
	v_exp_f32_e32 v109, v109
	v_pk_mul_f32 v[110:111], v[52:53], v[16:17] op_sel_hi:[0,1]
	v_pk_mul_f32 v[108:109], v[30:31], v[108:109]
	v_exp_f32_e32 v110, v110
	v_pk_fma_f32 v[30:31], v[112:113], s[44:45], v[108:109] op_sel_hi:[0,1,1]
	v_exp_f32_e32 v111, v111
	v_pk_fma_f32 v[114:115], s[60:61], v[30:31], v[114:115]
	v_pk_mul_f32 v[110:111], v[32:33], v[110:111]
	v_cvt_f32_f16_e32 v117, v63
	v_pk_fma_f32 v[32:33], v[112:113], s[46:47], v[110:111] op_sel_hi:[0,1,1]
	s_nop 0
	v_pk_fma_f32 v[114:115], s[62:63], v[32:33], v[114:115]
	s_nop 0
	v_add_f32_e32 v116, v114, v115
	v_fmac_f32_e32 v116, v98, v113
	v_mul_f32_e32 v116, v116, v117
	v_fma_mixlo_f16 v116, v116, s30, 0
	global_store_short v99, v116, s[26:27]
	s_add_u32 s26, s26, 0x1000
	s_addc_u32 s27, s27, 0
	s_waitcnt lgkmcnt(0)
	s_load_dwordx16 s[32:47], s[24:25], 0x600
	s_load_dwordx16 s[48:63], s[24:25], 0x640
	v_cvt_f32_f16_sdwa v113, v59 dst_sel:DWORD dst_unused:UNUSED_PAD src0_sel:WORD_1
	s_nop 0
	v_mul_f32_e32 v113, s29, v113
	v_mul_f32_e32 v112, v53, v113
	v_pk_mul_f32 v[104:105], v[52:53], v[2:3] op_sel:[1,0]
	v_pk_mul_f32 v[106:107], v[52:53], v[4:5] op_sel:[1,0]
	v_exp_f32_e32 v104, v104
	v_exp_f32_e32 v105, v105
	v_exp_f32_e32 v106, v106
	v_pk_mul_f32 v[104:105], v[18:19], v[104:105]
	v_exp_f32_e32 v107, v107
	v_pk_fma_f32 v[18:19], v[112:113], s[64:65], v[104:105] op_sel_hi:[0,1,1]
	v_pk_mul_f32 v[106:107], v[20:21], v[106:107]
	v_pk_fma_f32 v[114:115], s[80:81], v[18:19], 0 op_sel_hi:[1,1,0]
	v_pk_fma_f32 v[20:21], v[112:113], s[66:67], v[106:107] op_sel_hi:[0,1,1]
	v_pk_mul_f32 v[108:109], v[52:53], v[6:7] op_sel:[1,0]
	v_pk_fma_f32 v[114:115], s[82:83], v[20:21], v[114:115]
	v_exp_f32_e32 v108, v108
	v_exp_f32_e32 v109, v109
	v_pk_mul_f32 v[110:111], v[52:53], v[8:9] op_sel:[1,0]
	v_pk_mul_f32 v[108:109], v[22:23], v[108:109]
	v_exp_f32_e32 v110, v110
	v_pk_fma_f32 v[22:23], v[112:113], s[68:69], v[108:109] op_sel_hi:[0,1,1]
	v_exp_f32_e32 v111, v111
	v_pk_fma_f32 v[114:115], s[84:85], v[22:23], v[114:115]
	v_pk_mul_f32 v[110:111], v[24:25], v[110:111]
	v_pk_mul_f32 v[104:105], v[52:53], v[10:11] op_sel:[1,0]
	v_pk_fma_f32 v[24:25], v[112:113], s[70:71], v[110:111] op_sel_hi:[0,1,1]
	v_exp_f32_e32 v104, v104
	v_pk_fma_f32 v[114:115], s[86:87], v[24:25], v[114:115]
	v_exp_f32_e32 v105, v105
	v_pk_mul_f32 v[106:107], v[52:53], v[12:13] op_sel:[1,0]
	v_pk_mul_f32 v[104:105], v[26:27], v[104:105]
	v_exp_f32_e32 v106, v106
	v_pk_fma_f32 v[26:27], v[112:113], s[72:73], v[104:105] op_sel_hi:[0,1,1]
	v_exp_f32_e32 v107, v107
	v_pk_fma_f32 v[114:115], s[88:89], v[26:27], v[114:115]
	v_pk_mul_f32 v[106:107], v[28:29], v[106:107]
	v_pk_mul_f32 v[108:109], v[52:53], v[14:15] op_sel:[1,0]
	v_pk_fma_f32 v[28:29], v[112:113], s[74:75], v[106:107] op_sel_hi:[0,1,1]
	v_exp_f32_e32 v108, v108
	v_pk_fma_f32 v[114:115], s[90:91], v[28:29], v[114:115]
	v_exp_f32_e32 v109, v109
	v_pk_mul_f32 v[110:111], v[52:53], v[16:17] op_sel:[1,0]
	v_pk_mul_f32 v[108:109], v[30:31], v[108:109]
	v_exp_f32_e32 v110, v110
	v_pk_fma_f32 v[30:31], v[112:113], s[76:77], v[108:109] op_sel_hi:[0,1,1]
	v_exp_f32_e32 v111, v111
	v_pk_fma_f32 v[114:115], s[92:93], v[30:31], v[114:115]
	v_pk_mul_f32 v[110:111], v[32:33], v[110:111]
	v_cvt_f32_f16_sdwa v117, v63 dst_sel:DWORD dst_unused:UNUSED_PAD src0_sel:WORD_1
	v_pk_fma_f32 v[32:33], v[112:113], s[78:79], v[110:111] op_sel_hi:[0,1,1]
	s_nop 0
	v_pk_fma_f32 v[114:115], s[94:95], v[32:33], v[114:115]
	s_nop 0
	v_add_f32_e32 v116, v114, v115
	v_fmac_f32_e32 v116, v98, v113
	v_mul_f32_e32 v116, v116, v117
	v_fma_mixlo_f16 v116, v116, s30, 0
	global_store_short v99, v116, s[26:27]
	s_add_u32 s26, s26, 0x1000
	s_addc_u32 s27, s27, 0
	s_waitcnt lgkmcnt(0)
	s_load_dwordx16 s[64:79], s[24:25], 0x680
	s_load_dwordx16 s[80:95], s[24:25], 0x6c0
	v_cvt_f32_f16_e32 v113, v60
	v_mul_f32_e32 v113, s29, v113
	v_mul_f32_e32 v112, v54, v113
	v_pk_mul_f32 v[104:105], v[54:55], v[2:3] op_sel_hi:[0,1]
	v_pk_mul_f32 v[106:107], v[54:55], v[4:5] op_sel_hi:[0,1]
	v_exp_f32_e32 v104, v104
	v_exp_f32_e32 v105, v105
	v_exp_f32_e32 v106, v106
	v_pk_mul_f32 v[104:105], v[18:19], v[104:105]
	v_exp_f32_e32 v107, v107
	v_pk_fma_f32 v[18:19], v[112:113], s[32:33], v[104:105] op_sel_hi:[0,1,1]
	v_pk_mul_f32 v[106:107], v[20:21], v[106:107]
	v_pk_fma_f32 v[114:115], s[48:49], v[18:19], 0 op_sel_hi:[1,1,0]
	v_pk_fma_f32 v[20:21], v[112:113], s[34:35], v[106:107] op_sel_hi:[0,1,1]
	v_pk_mul_f32 v[108:109], v[54:55], v[6:7] op_sel_hi:[0,1]
	v_pk_fma_f32 v[114:115], s[50:51], v[20:21], v[114:115]
	v_exp_f32_e32 v108, v108
	v_exp_f32_e32 v109, v109
	v_pk_mul_f32 v[110:111], v[54:55], v[8:9] op_sel_hi:[0,1]
	v_pk_mul_f32 v[108:109], v[22:23], v[108:109]
	v_exp_f32_e32 v110, v110
	v_pk_fma_f32 v[22:23], v[112:113], s[36:37], v[108:109] op_sel_hi:[0,1,1]
	v_exp_f32_e32 v111, v111
	v_pk_fma_f32 v[114:115], s[52:53], v[22:23], v[114:115]
	v_pk_mul_f32 v[110:111], v[24:25], v[110:111]
	v_pk_mul_f32 v[104:105], v[54:55], v[10:11] op_sel_hi:[0,1]
	v_pk_fma_f32 v[24:25], v[112:113], s[38:39], v[110:111] op_sel_hi:[0,1,1]
	v_exp_f32_e32 v104, v104
	v_pk_fma_f32 v[114:115], s[54:55], v[24:25], v[114:115]
	v_exp_f32_e32 v105, v105
	v_pk_mul_f32 v[106:107], v[54:55], v[12:13] op_sel_hi:[0,1]
	v_pk_mul_f32 v[104:105], v[26:27], v[104:105]
	v_exp_f32_e32 v106, v106
	v_pk_fma_f32 v[26:27], v[112:113], s[40:41], v[104:105] op_sel_hi:[0,1,1]
	v_exp_f32_e32 v107, v107
	v_pk_fma_f32 v[114:115], s[56:57], v[26:27], v[114:115]
	v_pk_mul_f32 v[106:107], v[28:29], v[106:107]
	v_pk_mul_f32 v[108:109], v[54:55], v[14:15] op_sel_hi:[0,1]
	v_pk_fma_f32 v[28:29], v[112:113], s[42:43], v[106:107] op_sel_hi:[0,1,1]
	v_exp_f32_e32 v108, v108
	v_pk_fma_f32 v[114:115], s[58:59], v[28:29], v[114:115]
	v_exp_f32_e32 v109, v109
	v_pk_mul_f32 v[110:111], v[54:55], v[16:17] op_sel_hi:[0,1]
	v_pk_mul_f32 v[108:109], v[30:31], v[108:109]
	v_exp_f32_e32 v110, v110
	v_pk_fma_f32 v[30:31], v[112:113], s[44:45], v[108:109] op_sel_hi:[0,1,1]
	v_exp_f32_e32 v111, v111
	v_pk_fma_f32 v[114:115], s[60:61], v[30:31], v[114:115]
	v_pk_mul_f32 v[110:111], v[32:33], v[110:111]
	v_cvt_f32_f16_e32 v117, v64
	v_pk_fma_f32 v[32:33], v[112:113], s[46:47], v[110:111] op_sel_hi:[0,1,1]
	s_nop 0
	v_pk_fma_f32 v[114:115], s[62:63], v[32:33], v[114:115]
	s_nop 0
	v_add_f32_e32 v116, v114, v115
	v_fmac_f32_e32 v116, v98, v113
	v_mul_f32_e32 v116, v116, v117
	v_fma_mixlo_f16 v116, v116, s30, 0
	global_store_short v99, v116, s[26:27]
	s_add_u32 s26, s26, 0x1000
	s_addc_u32 s27, s27, 0
	s_waitcnt lgkmcnt(0)
	s_load_dwordx16 s[32:47], s[24:25], 0x700
	s_load_dwordx16 s[48:63], s[24:25], 0x740
	v_cvt_f32_f16_sdwa v113, v60 dst_sel:DWORD dst_unused:UNUSED_PAD src0_sel:WORD_1
	s_nop 0
	v_mul_f32_e32 v113, s29, v113
	v_mul_f32_e32 v112, v55, v113
	v_pk_mul_f32 v[104:105], v[54:55], v[2:3] op_sel:[1,0]
	v_pk_mul_f32 v[106:107], v[54:55], v[4:5] op_sel:[1,0]
	v_exp_f32_e32 v104, v104
	v_exp_f32_e32 v105, v105
	v_exp_f32_e32 v106, v106
	v_pk_mul_f32 v[104:105], v[18:19], v[104:105]
	v_exp_f32_e32 v107, v107
	v_pk_fma_f32 v[18:19], v[112:113], s[64:65], v[104:105] op_sel_hi:[0,1,1]
	v_pk_mul_f32 v[106:107], v[20:21], v[106:107]
	v_pk_fma_f32 v[114:115], s[80:81], v[18:19], 0 op_sel_hi:[1,1,0]
	v_pk_fma_f32 v[20:21], v[112:113], s[66:67], v[106:107] op_sel_hi:[0,1,1]
	v_pk_mul_f32 v[108:109], v[54:55], v[6:7] op_sel:[1,0]
	v_pk_fma_f32 v[114:115], s[82:83], v[20:21], v[114:115]
	v_exp_f32_e32 v108, v108
	v_exp_f32_e32 v109, v109
	v_pk_mul_f32 v[110:111], v[54:55], v[8:9] op_sel:[1,0]
	v_pk_mul_f32 v[108:109], v[22:23], v[108:109]
	v_exp_f32_e32 v110, v110
	v_pk_fma_f32 v[22:23], v[112:113], s[68:69], v[108:109] op_sel_hi:[0,1,1]
	v_exp_f32_e32 v111, v111
	v_pk_fma_f32 v[114:115], s[84:85], v[22:23], v[114:115]
	v_pk_mul_f32 v[110:111], v[24:25], v[110:111]
	v_pk_mul_f32 v[104:105], v[54:55], v[10:11] op_sel:[1,0]
	v_pk_fma_f32 v[24:25], v[112:113], s[70:71], v[110:111] op_sel_hi:[0,1,1]
	v_exp_f32_e32 v104, v104
	v_pk_fma_f32 v[114:115], s[86:87], v[24:25], v[114:115]
	v_exp_f32_e32 v105, v105
	v_pk_mul_f32 v[106:107], v[54:55], v[12:13] op_sel:[1,0]
	v_pk_mul_f32 v[104:105], v[26:27], v[104:105]
	v_exp_f32_e32 v106, v106
	v_pk_fma_f32 v[26:27], v[112:113], s[72:73], v[104:105] op_sel_hi:[0,1,1]
	v_exp_f32_e32 v107, v107
	v_pk_fma_f32 v[114:115], s[88:89], v[26:27], v[114:115]
	v_pk_mul_f32 v[106:107], v[28:29], v[106:107]
	v_pk_mul_f32 v[108:109], v[54:55], v[14:15] op_sel:[1,0]
	v_pk_fma_f32 v[28:29], v[112:113], s[74:75], v[106:107] op_sel_hi:[0,1,1]
	v_exp_f32_e32 v108, v108
	v_pk_fma_f32 v[114:115], s[90:91], v[28:29], v[114:115]
	v_exp_f32_e32 v109, v109
	v_pk_mul_f32 v[110:111], v[54:55], v[16:17] op_sel:[1,0]
	v_pk_mul_f32 v[108:109], v[30:31], v[108:109]
	v_exp_f32_e32 v110, v110
	v_pk_fma_f32 v[30:31], v[112:113], s[76:77], v[108:109] op_sel_hi:[0,1,1]
	v_exp_f32_e32 v111, v111
	v_pk_fma_f32 v[114:115], s[92:93], v[30:31], v[114:115]
	v_pk_mul_f32 v[110:111], v[32:33], v[110:111]
	v_cvt_f32_f16_sdwa v117, v64 dst_sel:DWORD dst_unused:UNUSED_PAD src0_sel:WORD_1
	v_pk_fma_f32 v[32:33], v[112:113], s[78:79], v[110:111] op_sel_hi:[0,1,1]
	s_nop 0
	v_pk_fma_f32 v[114:115], s[94:95], v[32:33], v[114:115]
	s_nop 0
	v_add_f32_e32 v116, v114, v115
	v_fmac_f32_e32 v116, v98, v113
	v_mul_f32_e32 v116, v116, v117
	v_fma_mixlo_f16 v116, v116, s30, 0
	global_store_short v99, v116, s[26:27]
	s_add_u32 s26, s26, 0x1000
	s_addc_u32 s27, s27, 0
	s_waitcnt lgkmcnt(0)
	s_load_dwordx16 s[64:79], s[24:25], 0x780
	s_load_dwordx16 s[80:95], s[24:25], 0x7c0
	v_cvt_f32_f16_e32 v113, v61
	v_mul_f32_e32 v113, s29, v113
	v_mul_f32_e32 v112, v56, v113
	v_pk_mul_f32 v[104:105], v[56:57], v[2:3] op_sel_hi:[0,1]
	v_pk_mul_f32 v[106:107], v[56:57], v[4:5] op_sel_hi:[0,1]
	v_exp_f32_e32 v104, v104
	v_exp_f32_e32 v105, v105
	v_exp_f32_e32 v106, v106
	v_pk_mul_f32 v[104:105], v[18:19], v[104:105]
	v_exp_f32_e32 v107, v107
	v_pk_fma_f32 v[18:19], v[112:113], s[32:33], v[104:105] op_sel_hi:[0,1,1]
	v_pk_mul_f32 v[106:107], v[20:21], v[106:107]
	v_pk_fma_f32 v[114:115], s[48:49], v[18:19], 0 op_sel_hi:[1,1,0]
	v_pk_fma_f32 v[20:21], v[112:113], s[34:35], v[106:107] op_sel_hi:[0,1,1]
	v_pk_mul_f32 v[108:109], v[56:57], v[6:7] op_sel_hi:[0,1]
	v_pk_fma_f32 v[114:115], s[50:51], v[20:21], v[114:115]
	v_exp_f32_e32 v108, v108
	v_exp_f32_e32 v109, v109
	v_pk_mul_f32 v[110:111], v[56:57], v[8:9] op_sel_hi:[0,1]
	v_pk_mul_f32 v[108:109], v[22:23], v[108:109]
	v_exp_f32_e32 v110, v110
	v_pk_fma_f32 v[22:23], v[112:113], s[36:37], v[108:109] op_sel_hi:[0,1,1]
	v_exp_f32_e32 v111, v111
	v_pk_fma_f32 v[114:115], s[52:53], v[22:23], v[114:115]
	v_pk_mul_f32 v[110:111], v[24:25], v[110:111]
	v_pk_mul_f32 v[104:105], v[56:57], v[10:11] op_sel_hi:[0,1]
	v_pk_fma_f32 v[24:25], v[112:113], s[38:39], v[110:111] op_sel_hi:[0,1,1]
	v_exp_f32_e32 v104, v104
	v_pk_fma_f32 v[114:115], s[54:55], v[24:25], v[114:115]
	v_exp_f32_e32 v105, v105
	v_pk_mul_f32 v[106:107], v[56:57], v[12:13] op_sel_hi:[0,1]
	v_pk_mul_f32 v[104:105], v[26:27], v[104:105]
	v_exp_f32_e32 v106, v106
	v_pk_fma_f32 v[26:27], v[112:113], s[40:41], v[104:105] op_sel_hi:[0,1,1]
	v_exp_f32_e32 v107, v107
	v_pk_fma_f32 v[114:115], s[56:57], v[26:27], v[114:115]
	v_pk_mul_f32 v[106:107], v[28:29], v[106:107]
	v_pk_mul_f32 v[108:109], v[56:57], v[14:15] op_sel_hi:[0,1]
	v_pk_fma_f32 v[28:29], v[112:113], s[42:43], v[106:107] op_sel_hi:[0,1,1]
	v_exp_f32_e32 v108, v108
	v_pk_fma_f32 v[114:115], s[58:59], v[28:29], v[114:115]
	v_exp_f32_e32 v109, v109
	v_pk_mul_f32 v[110:111], v[56:57], v[16:17] op_sel_hi:[0,1]
	v_pk_mul_f32 v[108:109], v[30:31], v[108:109]
	v_exp_f32_e32 v110, v110
	v_pk_fma_f32 v[30:31], v[112:113], s[44:45], v[108:109] op_sel_hi:[0,1,1]
	v_exp_f32_e32 v111, v111
	v_pk_fma_f32 v[114:115], s[60:61], v[30:31], v[114:115]
	v_pk_mul_f32 v[110:111], v[32:33], v[110:111]
	v_cvt_f32_f16_e32 v117, v65
	v_pk_fma_f32 v[32:33], v[112:113], s[46:47], v[110:111] op_sel_hi:[0,1,1]
	s_nop 0
	v_pk_fma_f32 v[114:115], s[62:63], v[32:33], v[114:115]
	s_nop 0
	v_add_f32_e32 v116, v114, v115
	v_fmac_f32_e32 v116, v98, v113
	v_mul_f32_e32 v116, v116, v117
	v_fma_mixlo_f16 v116, v116, s30, 0
	global_store_short v99, v116, s[26:27]
	s_add_u32 s26, s26, 0x1000
	s_addc_u32 s27, s27, 0
	s_waitcnt lgkmcnt(0)
	s_load_dwordx16 s[32:47], s[24:25], 0x800
	s_load_dwordx16 s[48:63], s[24:25], 0x840
	v_cvt_f32_f16_sdwa v113, v61 dst_sel:DWORD dst_unused:UNUSED_PAD src0_sel:WORD_1
	s_nop 0
	v_mul_f32_e32 v113, s29, v113
	v_mul_f32_e32 v112, v57, v113
	v_pk_mul_f32 v[104:105], v[56:57], v[2:3] op_sel:[1,0]
	v_pk_mul_f32 v[106:107], v[56:57], v[4:5] op_sel:[1,0]
	v_exp_f32_e32 v104, v104
	v_exp_f32_e32 v105, v105
	v_exp_f32_e32 v106, v106
	v_pk_mul_f32 v[104:105], v[18:19], v[104:105]
	v_exp_f32_e32 v107, v107
	v_pk_fma_f32 v[18:19], v[112:113], s[64:65], v[104:105] op_sel_hi:[0,1,1]
	v_pk_mul_f32 v[106:107], v[20:21], v[106:107]
	v_pk_fma_f32 v[114:115], s[80:81], v[18:19], 0 op_sel_hi:[1,1,0]
	v_pk_fma_f32 v[20:21], v[112:113], s[66:67], v[106:107] op_sel_hi:[0,1,1]
	v_pk_mul_f32 v[108:109], v[56:57], v[6:7] op_sel:[1,0]
	v_pk_fma_f32 v[114:115], s[82:83], v[20:21], v[114:115]
	v_exp_f32_e32 v108, v108
	v_exp_f32_e32 v109, v109
	v_pk_mul_f32 v[110:111], v[56:57], v[8:9] op_sel:[1,0]
	v_pk_mul_f32 v[108:109], v[22:23], v[108:109]
	v_exp_f32_e32 v110, v110
	v_pk_fma_f32 v[22:23], v[112:113], s[68:69], v[108:109] op_sel_hi:[0,1,1]
	v_exp_f32_e32 v111, v111
	v_pk_fma_f32 v[114:115], s[84:85], v[22:23], v[114:115]
	v_pk_mul_f32 v[110:111], v[24:25], v[110:111]
	v_pk_mul_f32 v[104:105], v[56:57], v[10:11] op_sel:[1,0]
	v_pk_fma_f32 v[24:25], v[112:113], s[70:71], v[110:111] op_sel_hi:[0,1,1]
	v_exp_f32_e32 v104, v104
	v_pk_fma_f32 v[114:115], s[86:87], v[24:25], v[114:115]
	v_exp_f32_e32 v105, v105
	v_pk_mul_f32 v[106:107], v[56:57], v[12:13] op_sel:[1,0]
	v_pk_mul_f32 v[104:105], v[26:27], v[104:105]
	v_exp_f32_e32 v106, v106
	v_pk_fma_f32 v[26:27], v[112:113], s[72:73], v[104:105] op_sel_hi:[0,1,1]
	v_exp_f32_e32 v107, v107
	v_pk_fma_f32 v[114:115], s[88:89], v[26:27], v[114:115]
	v_pk_mul_f32 v[106:107], v[28:29], v[106:107]
	v_pk_mul_f32 v[108:109], v[56:57], v[14:15] op_sel:[1,0]
	v_pk_fma_f32 v[28:29], v[112:113], s[74:75], v[106:107] op_sel_hi:[0,1,1]
	v_exp_f32_e32 v108, v108
	v_pk_fma_f32 v[114:115], s[90:91], v[28:29], v[114:115]
	v_exp_f32_e32 v109, v109
	v_pk_mul_f32 v[110:111], v[56:57], v[16:17] op_sel:[1,0]
	v_pk_mul_f32 v[108:109], v[30:31], v[108:109]
	v_exp_f32_e32 v110, v110
	v_pk_fma_f32 v[30:31], v[112:113], s[76:77], v[108:109] op_sel_hi:[0,1,1]
	v_exp_f32_e32 v111, v111
	v_pk_fma_f32 v[114:115], s[92:93], v[30:31], v[114:115]
	v_pk_mul_f32 v[110:111], v[32:33], v[110:111]
	v_cvt_f32_f16_sdwa v117, v65 dst_sel:DWORD dst_unused:UNUSED_PAD src0_sel:WORD_1
	v_pk_fma_f32 v[32:33], v[112:113], s[78:79], v[110:111] op_sel_hi:[0,1,1]
	s_nop 0
	v_pk_fma_f32 v[114:115], s[94:95], v[32:33], v[114:115]
	s_nop 0
	v_add_f32_e32 v116, v114, v115
	v_fmac_f32_e32 v116, v98, v113
	v_mul_f32_e32 v116, v116, v117
	v_fma_mixlo_f16 v116, v116, s30, 0
	global_store_short v99, v116, s[26:27]
	s_add_u32 s26, s26, 0x1000
	s_addc_u32 s27, s27, 0
	s_waitcnt vmcnt(21)
	s_waitcnt lgkmcnt(0)
	s_load_dwordx16 s[64:79], s[24:25], 0x880
	s_load_dwordx16 s[80:95], s[24:25], 0x8c0
	v_cvt_f32_f16_e32 v113, v74
	v_mul_f32_e32 v113, s29, v113
	v_mul_f32_e32 v112, v66, v113
	v_pk_mul_f32 v[104:105], v[66:67], v[2:3] op_sel_hi:[0,1]
	v_pk_mul_f32 v[106:107], v[66:67], v[4:5] op_sel_hi:[0,1]
	v_exp_f32_e32 v104, v104
	v_exp_f32_e32 v105, v105
	v_exp_f32_e32 v106, v106
	v_pk_mul_f32 v[104:105], v[18:19], v[104:105]
	v_exp_f32_e32 v107, v107
	v_pk_fma_f32 v[18:19], v[112:113], s[32:33], v[104:105] op_sel_hi:[0,1,1]
	v_pk_mul_f32 v[106:107], v[20:21], v[106:107]
	v_pk_fma_f32 v[114:115], s[48:49], v[18:19], 0 op_sel_hi:[1,1,0]
	v_pk_fma_f32 v[20:21], v[112:113], s[34:35], v[106:107] op_sel_hi:[0,1,1]
	v_pk_mul_f32 v[108:109], v[66:67], v[6:7] op_sel_hi:[0,1]
	v_pk_fma_f32 v[114:115], s[50:51], v[20:21], v[114:115]
	v_exp_f32_e32 v108, v108
	v_exp_f32_e32 v109, v109
	v_pk_mul_f32 v[110:111], v[66:67], v[8:9] op_sel_hi:[0,1]
	v_pk_mul_f32 v[108:109], v[22:23], v[108:109]
	v_exp_f32_e32 v110, v110
	v_pk_fma_f32 v[22:23], v[112:113], s[36:37], v[108:109] op_sel_hi:[0,1,1]
	v_exp_f32_e32 v111, v111
	v_pk_fma_f32 v[114:115], s[52:53], v[22:23], v[114:115]
	v_pk_mul_f32 v[110:111], v[24:25], v[110:111]
	v_pk_mul_f32 v[104:105], v[66:67], v[10:11] op_sel_hi:[0,1]
	v_pk_fma_f32 v[24:25], v[112:113], s[38:39], v[110:111] op_sel_hi:[0,1,1]
	v_exp_f32_e32 v104, v104
	v_pk_fma_f32 v[114:115], s[54:55], v[24:25], v[114:115]
	v_exp_f32_e32 v105, v105
	v_pk_mul_f32 v[106:107], v[66:67], v[12:13] op_sel_hi:[0,1]
	v_pk_mul_f32 v[104:105], v[26:27], v[104:105]
	v_exp_f32_e32 v106, v106
	v_pk_fma_f32 v[26:27], v[112:113], s[40:41], v[104:105] op_sel_hi:[0,1,1]
	v_exp_f32_e32 v107, v107
	v_pk_fma_f32 v[114:115], s[56:57], v[26:27], v[114:115]
	v_pk_mul_f32 v[106:107], v[28:29], v[106:107]
	v_pk_mul_f32 v[108:109], v[66:67], v[14:15] op_sel_hi:[0,1]
	v_pk_fma_f32 v[28:29], v[112:113], s[42:43], v[106:107] op_sel_hi:[0,1,1]
	v_exp_f32_e32 v108, v108
	v_pk_fma_f32 v[114:115], s[58:59], v[28:29], v[114:115]
	v_exp_f32_e32 v109, v109
	v_pk_mul_f32 v[110:111], v[66:67], v[16:17] op_sel_hi:[0,1]
	v_pk_mul_f32 v[108:109], v[30:31], v[108:109]
	v_exp_f32_e32 v110, v110
	v_pk_fma_f32 v[30:31], v[112:113], s[44:45], v[108:109] op_sel_hi:[0,1,1]
	v_exp_f32_e32 v111, v111
	v_pk_fma_f32 v[114:115], s[60:61], v[30:31], v[114:115]
	v_pk_mul_f32 v[110:111], v[32:33], v[110:111]
	v_cvt_f32_f16_e32 v117, v78
	v_pk_fma_f32 v[32:33], v[112:113], s[46:47], v[110:111] op_sel_hi:[0,1,1]
	s_nop 0
	v_pk_fma_f32 v[114:115], s[62:63], v[32:33], v[114:115]
	s_nop 0
	v_add_f32_e32 v116, v114, v115
	v_fmac_f32_e32 v116, v98, v113
	v_mul_f32_e32 v116, v116, v117
	v_fma_mixlo_f16 v116, v116, s30, 0
	global_store_short v99, v116, s[26:27]
	s_add_u32 s26, s26, 0x1000
	s_addc_u32 s27, s27, 0
	s_waitcnt lgkmcnt(0)
	s_load_dwordx16 s[32:47], s[24:25], 0x900
	s_load_dwordx16 s[48:63], s[24:25], 0x940
	v_cvt_f32_f16_sdwa v113, v74 dst_sel:DWORD dst_unused:UNUSED_PAD src0_sel:WORD_1
	s_nop 0
	v_mul_f32_e32 v113, s29, v113
	v_mul_f32_e32 v112, v67, v113
	v_pk_mul_f32 v[104:105], v[66:67], v[2:3] op_sel:[1,0]
	v_pk_mul_f32 v[106:107], v[66:67], v[4:5] op_sel:[1,0]
	v_exp_f32_e32 v104, v104
	v_exp_f32_e32 v105, v105
	v_exp_f32_e32 v106, v106
	v_pk_mul_f32 v[104:105], v[18:19], v[104:105]
	v_exp_f32_e32 v107, v107
	v_pk_fma_f32 v[18:19], v[112:113], s[64:65], v[104:105] op_sel_hi:[0,1,1]
	v_pk_mul_f32 v[106:107], v[20:21], v[106:107]
	v_pk_fma_f32 v[114:115], s[80:81], v[18:19], 0 op_sel_hi:[1,1,0]
	v_pk_fma_f32 v[20:21], v[112:113], s[66:67], v[106:107] op_sel_hi:[0,1,1]
	v_pk_mul_f32 v[108:109], v[66:67], v[6:7] op_sel:[1,0]
	v_pk_fma_f32 v[114:115], s[82:83], v[20:21], v[114:115]
	v_exp_f32_e32 v108, v108
	v_exp_f32_e32 v109, v109
	v_pk_mul_f32 v[110:111], v[66:67], v[8:9] op_sel:[1,0]
	v_pk_mul_f32 v[108:109], v[22:23], v[108:109]
	v_exp_f32_e32 v110, v110
	v_pk_fma_f32 v[22:23], v[112:113], s[68:69], v[108:109] op_sel_hi:[0,1,1]
	v_exp_f32_e32 v111, v111
	v_pk_fma_f32 v[114:115], s[84:85], v[22:23], v[114:115]
	v_pk_mul_f32 v[110:111], v[24:25], v[110:111]
	v_pk_mul_f32 v[104:105], v[66:67], v[10:11] op_sel:[1,0]
	v_pk_fma_f32 v[24:25], v[112:113], s[70:71], v[110:111] op_sel_hi:[0,1,1]
	v_exp_f32_e32 v104, v104
	v_pk_fma_f32 v[114:115], s[86:87], v[24:25], v[114:115]
	v_exp_f32_e32 v105, v105
	v_pk_mul_f32 v[106:107], v[66:67], v[12:13] op_sel:[1,0]
	v_pk_mul_f32 v[104:105], v[26:27], v[104:105]
	v_exp_f32_e32 v106, v106
	v_pk_fma_f32 v[26:27], v[112:113], s[72:73], v[104:105] op_sel_hi:[0,1,1]
	v_exp_f32_e32 v107, v107
	v_pk_fma_f32 v[114:115], s[88:89], v[26:27], v[114:115]
	v_pk_mul_f32 v[106:107], v[28:29], v[106:107]
	v_pk_mul_f32 v[108:109], v[66:67], v[14:15] op_sel:[1,0]
	v_pk_fma_f32 v[28:29], v[112:113], s[74:75], v[106:107] op_sel_hi:[0,1,1]
	v_exp_f32_e32 v108, v108
	v_pk_fma_f32 v[114:115], s[90:91], v[28:29], v[114:115]
	v_exp_f32_e32 v109, v109
	v_pk_mul_f32 v[110:111], v[66:67], v[16:17] op_sel:[1,0]
	v_pk_mul_f32 v[108:109], v[30:31], v[108:109]
	v_exp_f32_e32 v110, v110
	v_pk_fma_f32 v[30:31], v[112:113], s[76:77], v[108:109] op_sel_hi:[0,1,1]
	v_exp_f32_e32 v111, v111
	v_pk_fma_f32 v[114:115], s[92:93], v[30:31], v[114:115]
	v_pk_mul_f32 v[110:111], v[32:33], v[110:111]
	v_cvt_f32_f16_sdwa v117, v78 dst_sel:DWORD dst_unused:UNUSED_PAD src0_sel:WORD_1
	v_pk_fma_f32 v[32:33], v[112:113], s[78:79], v[110:111] op_sel_hi:[0,1,1]
	s_nop 0
	v_pk_fma_f32 v[114:115], s[94:95], v[32:33], v[114:115]
	s_nop 0
	v_add_f32_e32 v116, v114, v115
	v_fmac_f32_e32 v116, v98, v113
	v_mul_f32_e32 v116, v116, v117
	v_fma_mixlo_f16 v116, v116, s30, 0
	global_store_short v99, v116, s[26:27]
	s_add_u32 s26, s26, 0x1000
	s_addc_u32 s27, s27, 0
	s_waitcnt lgkmcnt(0)
	s_load_dwordx16 s[64:79], s[24:25], 0x980
	s_load_dwordx16 s[80:95], s[24:25], 0x9c0
	v_cvt_f32_f16_e32 v113, v75
	v_mul_f32_e32 v113, s29, v113
	v_mul_f32_e32 v112, v68, v113
	v_pk_mul_f32 v[104:105], v[68:69], v[2:3] op_sel_hi:[0,1]
	v_pk_mul_f32 v[106:107], v[68:69], v[4:5] op_sel_hi:[0,1]
	v_exp_f32_e32 v104, v104
	v_exp_f32_e32 v105, v105
	v_exp_f32_e32 v106, v106
	v_pk_mul_f32 v[104:105], v[18:19], v[104:105]
	v_exp_f32_e32 v107, v107
	v_pk_fma_f32 v[18:19], v[112:113], s[32:33], v[104:105] op_sel_hi:[0,1,1]
	v_pk_mul_f32 v[106:107], v[20:21], v[106:107]
	v_pk_fma_f32 v[114:115], s[48:49], v[18:19], 0 op_sel_hi:[1,1,0]
	v_pk_fma_f32 v[20:21], v[112:113], s[34:35], v[106:107] op_sel_hi:[0,1,1]
	v_pk_mul_f32 v[108:109], v[68:69], v[6:7] op_sel_hi:[0,1]
	v_pk_fma_f32 v[114:115], s[50:51], v[20:21], v[114:115]
	v_exp_f32_e32 v108, v108
	v_exp_f32_e32 v109, v109
	v_pk_mul_f32 v[110:111], v[68:69], v[8:9] op_sel_hi:[0,1]
	v_pk_mul_f32 v[108:109], v[22:23], v[108:109]
	v_exp_f32_e32 v110, v110
	v_pk_fma_f32 v[22:23], v[112:113], s[36:37], v[108:109] op_sel_hi:[0,1,1]
	v_exp_f32_e32 v111, v111
	v_pk_fma_f32 v[114:115], s[52:53], v[22:23], v[114:115]
	v_pk_mul_f32 v[110:111], v[24:25], v[110:111]
	v_pk_mul_f32 v[104:105], v[68:69], v[10:11] op_sel_hi:[0,1]
	v_pk_fma_f32 v[24:25], v[112:113], s[38:39], v[110:111] op_sel_hi:[0,1,1]
	v_exp_f32_e32 v104, v104
	v_pk_fma_f32 v[114:115], s[54:55], v[24:25], v[114:115]
	v_exp_f32_e32 v105, v105
	v_pk_mul_f32 v[106:107], v[68:69], v[12:13] op_sel_hi:[0,1]
	v_pk_mul_f32 v[104:105], v[26:27], v[104:105]
	v_exp_f32_e32 v106, v106
	v_pk_fma_f32 v[26:27], v[112:113], s[40:41], v[104:105] op_sel_hi:[0,1,1]
	v_exp_f32_e32 v107, v107
	v_pk_fma_f32 v[114:115], s[56:57], v[26:27], v[114:115]
	v_pk_mul_f32 v[106:107], v[28:29], v[106:107]
	v_pk_mul_f32 v[108:109], v[68:69], v[14:15] op_sel_hi:[0,1]
	v_pk_fma_f32 v[28:29], v[112:113], s[42:43], v[106:107] op_sel_hi:[0,1,1]
	v_exp_f32_e32 v108, v108
	v_pk_fma_f32 v[114:115], s[58:59], v[28:29], v[114:115]
	v_exp_f32_e32 v109, v109
	v_pk_mul_f32 v[110:111], v[68:69], v[16:17] op_sel_hi:[0,1]
	v_pk_mul_f32 v[108:109], v[30:31], v[108:109]
	v_exp_f32_e32 v110, v110
	v_pk_fma_f32 v[30:31], v[112:113], s[44:45], v[108:109] op_sel_hi:[0,1,1]
	v_exp_f32_e32 v111, v111
	v_pk_fma_f32 v[114:115], s[60:61], v[30:31], v[114:115]
	v_pk_mul_f32 v[110:111], v[32:33], v[110:111]
	v_cvt_f32_f16_e32 v117, v79
	v_pk_fma_f32 v[32:33], v[112:113], s[46:47], v[110:111] op_sel_hi:[0,1,1]
	s_nop 0
	v_pk_fma_f32 v[114:115], s[62:63], v[32:33], v[114:115]
	s_nop 0
	v_add_f32_e32 v116, v114, v115
	v_fmac_f32_e32 v116, v98, v113
	v_mul_f32_e32 v116, v116, v117
	v_fma_mixlo_f16 v116, v116, s30, 0
	global_store_short v99, v116, s[26:27]
	s_add_u32 s26, s26, 0x1000
	s_addc_u32 s27, s27, 0
	s_waitcnt lgkmcnt(0)
	s_load_dwordx16 s[32:47], s[24:25], 0xa00
	s_load_dwordx16 s[48:63], s[24:25], 0xa40
	v_cvt_f32_f16_sdwa v113, v75 dst_sel:DWORD dst_unused:UNUSED_PAD src0_sel:WORD_1
	s_nop 0
	v_mul_f32_e32 v113, s29, v113
	v_mul_f32_e32 v112, v69, v113
	v_pk_mul_f32 v[104:105], v[68:69], v[2:3] op_sel:[1,0]
	v_pk_mul_f32 v[106:107], v[68:69], v[4:5] op_sel:[1,0]
	v_exp_f32_e32 v104, v104
	v_exp_f32_e32 v105, v105
	v_exp_f32_e32 v106, v106
	v_pk_mul_f32 v[104:105], v[18:19], v[104:105]
	v_exp_f32_e32 v107, v107
	v_pk_fma_f32 v[18:19], v[112:113], s[64:65], v[104:105] op_sel_hi:[0,1,1]
	v_pk_mul_f32 v[106:107], v[20:21], v[106:107]
	v_pk_fma_f32 v[114:115], s[80:81], v[18:19], 0 op_sel_hi:[1,1,0]
	v_pk_fma_f32 v[20:21], v[112:113], s[66:67], v[106:107] op_sel_hi:[0,1,1]
	v_pk_mul_f32 v[108:109], v[68:69], v[6:7] op_sel:[1,0]
	v_pk_fma_f32 v[114:115], s[82:83], v[20:21], v[114:115]
	v_exp_f32_e32 v108, v108
	v_exp_f32_e32 v109, v109
	v_pk_mul_f32 v[110:111], v[68:69], v[8:9] op_sel:[1,0]
	v_pk_mul_f32 v[108:109], v[22:23], v[108:109]
	v_exp_f32_e32 v110, v110
	v_pk_fma_f32 v[22:23], v[112:113], s[68:69], v[108:109] op_sel_hi:[0,1,1]
	v_exp_f32_e32 v111, v111
	v_pk_fma_f32 v[114:115], s[84:85], v[22:23], v[114:115]
	v_pk_mul_f32 v[110:111], v[24:25], v[110:111]
	v_pk_mul_f32 v[104:105], v[68:69], v[10:11] op_sel:[1,0]
	v_pk_fma_f32 v[24:25], v[112:113], s[70:71], v[110:111] op_sel_hi:[0,1,1]
	v_exp_f32_e32 v104, v104
	v_pk_fma_f32 v[114:115], s[86:87], v[24:25], v[114:115]
	v_exp_f32_e32 v105, v105
	v_pk_mul_f32 v[106:107], v[68:69], v[12:13] op_sel:[1,0]
	v_pk_mul_f32 v[104:105], v[26:27], v[104:105]
	v_exp_f32_e32 v106, v106
	v_pk_fma_f32 v[26:27], v[112:113], s[72:73], v[104:105] op_sel_hi:[0,1,1]
	v_exp_f32_e32 v107, v107
	v_pk_fma_f32 v[114:115], s[88:89], v[26:27], v[114:115]
	v_pk_mul_f32 v[106:107], v[28:29], v[106:107]
	v_pk_mul_f32 v[108:109], v[68:69], v[14:15] op_sel:[1,0]
	v_pk_fma_f32 v[28:29], v[112:113], s[74:75], v[106:107] op_sel_hi:[0,1,1]
	v_exp_f32_e32 v108, v108
	v_pk_fma_f32 v[114:115], s[90:91], v[28:29], v[114:115]
	v_exp_f32_e32 v109, v109
	v_pk_mul_f32 v[110:111], v[68:69], v[16:17] op_sel:[1,0]
	v_pk_mul_f32 v[108:109], v[30:31], v[108:109]
	v_exp_f32_e32 v110, v110
	v_pk_fma_f32 v[30:31], v[112:113], s[76:77], v[108:109] op_sel_hi:[0,1,1]
	v_exp_f32_e32 v111, v111
	v_pk_fma_f32 v[114:115], s[92:93], v[30:31], v[114:115]
	v_pk_mul_f32 v[110:111], v[32:33], v[110:111]
	v_cvt_f32_f16_sdwa v117, v79 dst_sel:DWORD dst_unused:UNUSED_PAD src0_sel:WORD_1
	v_pk_fma_f32 v[32:33], v[112:113], s[78:79], v[110:111] op_sel_hi:[0,1,1]
	s_nop 0
	v_pk_fma_f32 v[114:115], s[94:95], v[32:33], v[114:115]
	s_nop 0
	v_add_f32_e32 v116, v114, v115
	v_fmac_f32_e32 v116, v98, v113
	v_mul_f32_e32 v116, v116, v117
	v_fma_mixlo_f16 v116, v116, s30, 0
	global_store_short v99, v116, s[26:27]
	s_add_u32 s26, s26, 0x1000
	s_addc_u32 s27, s27, 0
	s_waitcnt lgkmcnt(0)
	s_load_dwordx16 s[64:79], s[24:25], 0xa80
	s_load_dwordx16 s[80:95], s[24:25], 0xac0
	v_cvt_f32_f16_e32 v113, v76
	v_mul_f32_e32 v113, s29, v113
	v_mul_f32_e32 v112, v70, v113
	v_pk_mul_f32 v[104:105], v[70:71], v[2:3] op_sel_hi:[0,1]
	v_pk_mul_f32 v[106:107], v[70:71], v[4:5] op_sel_hi:[0,1]
	v_exp_f32_e32 v104, v104
	v_exp_f32_e32 v105, v105
	v_exp_f32_e32 v106, v106
	v_pk_mul_f32 v[104:105], v[18:19], v[104:105]
	v_exp_f32_e32 v107, v107
	v_pk_fma_f32 v[18:19], v[112:113], s[32:33], v[104:105] op_sel_hi:[0,1,1]
	v_pk_mul_f32 v[106:107], v[20:21], v[106:107]
	v_pk_fma_f32 v[114:115], s[48:49], v[18:19], 0 op_sel_hi:[1,1,0]
	v_pk_fma_f32 v[20:21], v[112:113], s[34:35], v[106:107] op_sel_hi:[0,1,1]
	v_pk_mul_f32 v[108:109], v[70:71], v[6:7] op_sel_hi:[0,1]
	v_pk_fma_f32 v[114:115], s[50:51], v[20:21], v[114:115]
	v_exp_f32_e32 v108, v108
	v_exp_f32_e32 v109, v109
	v_pk_mul_f32 v[110:111], v[70:71], v[8:9] op_sel_hi:[0,1]
	v_pk_mul_f32 v[108:109], v[22:23], v[108:109]
	v_exp_f32_e32 v110, v110
	v_pk_fma_f32 v[22:23], v[112:113], s[36:37], v[108:109] op_sel_hi:[0,1,1]
	v_exp_f32_e32 v111, v111
	v_pk_fma_f32 v[114:115], s[52:53], v[22:23], v[114:115]
	v_pk_mul_f32 v[110:111], v[24:25], v[110:111]
	v_pk_mul_f32 v[104:105], v[70:71], v[10:11] op_sel_hi:[0,1]
	v_pk_fma_f32 v[24:25], v[112:113], s[38:39], v[110:111] op_sel_hi:[0,1,1]
	v_exp_f32_e32 v104, v104
	v_pk_fma_f32 v[114:115], s[54:55], v[24:25], v[114:115]
	v_exp_f32_e32 v105, v105
	v_pk_mul_f32 v[106:107], v[70:71], v[12:13] op_sel_hi:[0,1]
	v_pk_mul_f32 v[104:105], v[26:27], v[104:105]
	v_exp_f32_e32 v106, v106
	v_pk_fma_f32 v[26:27], v[112:113], s[40:41], v[104:105] op_sel_hi:[0,1,1]
	v_exp_f32_e32 v107, v107
	v_pk_fma_f32 v[114:115], s[56:57], v[26:27], v[114:115]
	v_pk_mul_f32 v[106:107], v[28:29], v[106:107]
	v_pk_mul_f32 v[108:109], v[70:71], v[14:15] op_sel_hi:[0,1]
	v_pk_fma_f32 v[28:29], v[112:113], s[42:43], v[106:107] op_sel_hi:[0,1,1]
	v_exp_f32_e32 v108, v108
	v_pk_fma_f32 v[114:115], s[58:59], v[28:29], v[114:115]
	v_exp_f32_e32 v109, v109
	v_pk_mul_f32 v[110:111], v[70:71], v[16:17] op_sel_hi:[0,1]
	v_pk_mul_f32 v[108:109], v[30:31], v[108:109]
	v_exp_f32_e32 v110, v110
	v_pk_fma_f32 v[30:31], v[112:113], s[44:45], v[108:109] op_sel_hi:[0,1,1]
	v_exp_f32_e32 v111, v111
	v_pk_fma_f32 v[114:115], s[60:61], v[30:31], v[114:115]
	v_pk_mul_f32 v[110:111], v[32:33], v[110:111]
	v_cvt_f32_f16_e32 v117, v80
	v_pk_fma_f32 v[32:33], v[112:113], s[46:47], v[110:111] op_sel_hi:[0,1,1]
	s_nop 0
	v_pk_fma_f32 v[114:115], s[62:63], v[32:33], v[114:115]
	s_nop 0
	v_add_f32_e32 v116, v114, v115
	v_fmac_f32_e32 v116, v98, v113
	v_mul_f32_e32 v116, v116, v117
	v_fma_mixlo_f16 v116, v116, s30, 0
	global_store_short v99, v116, s[26:27]
	s_add_u32 s26, s26, 0x1000
	s_addc_u32 s27, s27, 0
	s_waitcnt lgkmcnt(0)
	s_load_dwordx16 s[32:47], s[24:25], 0xb00
	s_load_dwordx16 s[48:63], s[24:25], 0xb40
	v_cvt_f32_f16_sdwa v113, v76 dst_sel:DWORD dst_unused:UNUSED_PAD src0_sel:WORD_1
	s_nop 0
	v_mul_f32_e32 v113, s29, v113
	v_mul_f32_e32 v112, v71, v113
	v_pk_mul_f32 v[104:105], v[70:71], v[2:3] op_sel:[1,0]
	v_pk_mul_f32 v[106:107], v[70:71], v[4:5] op_sel:[1,0]
	v_exp_f32_e32 v104, v104
	v_exp_f32_e32 v105, v105
	v_exp_f32_e32 v106, v106
	v_pk_mul_f32 v[104:105], v[18:19], v[104:105]
	v_exp_f32_e32 v107, v107
	v_pk_fma_f32 v[18:19], v[112:113], s[64:65], v[104:105] op_sel_hi:[0,1,1]
	v_pk_mul_f32 v[106:107], v[20:21], v[106:107]
	v_pk_fma_f32 v[114:115], s[80:81], v[18:19], 0 op_sel_hi:[1,1,0]
	v_pk_fma_f32 v[20:21], v[112:113], s[66:67], v[106:107] op_sel_hi:[0,1,1]
	v_pk_mul_f32 v[108:109], v[70:71], v[6:7] op_sel:[1,0]
	v_pk_fma_f32 v[114:115], s[82:83], v[20:21], v[114:115]
	v_exp_f32_e32 v108, v108
	v_exp_f32_e32 v109, v109
	v_pk_mul_f32 v[110:111], v[70:71], v[8:9] op_sel:[1,0]
	v_pk_mul_f32 v[108:109], v[22:23], v[108:109]
	v_exp_f32_e32 v110, v110
	v_pk_fma_f32 v[22:23], v[112:113], s[68:69], v[108:109] op_sel_hi:[0,1,1]
	v_exp_f32_e32 v111, v111
	v_pk_fma_f32 v[114:115], s[84:85], v[22:23], v[114:115]
	v_pk_mul_f32 v[110:111], v[24:25], v[110:111]
	v_pk_mul_f32 v[104:105], v[70:71], v[10:11] op_sel:[1,0]
	v_pk_fma_f32 v[24:25], v[112:113], s[70:71], v[110:111] op_sel_hi:[0,1,1]
	v_exp_f32_e32 v104, v104
	v_pk_fma_f32 v[114:115], s[86:87], v[24:25], v[114:115]
	v_exp_f32_e32 v105, v105
	v_pk_mul_f32 v[106:107], v[70:71], v[12:13] op_sel:[1,0]
	v_pk_mul_f32 v[104:105], v[26:27], v[104:105]
	v_exp_f32_e32 v106, v106
	v_pk_fma_f32 v[26:27], v[112:113], s[72:73], v[104:105] op_sel_hi:[0,1,1]
	v_exp_f32_e32 v107, v107
	v_pk_fma_f32 v[114:115], s[88:89], v[26:27], v[114:115]
	v_pk_mul_f32 v[106:107], v[28:29], v[106:107]
	v_pk_mul_f32 v[108:109], v[70:71], v[14:15] op_sel:[1,0]
	v_pk_fma_f32 v[28:29], v[112:113], s[74:75], v[106:107] op_sel_hi:[0,1,1]
	v_exp_f32_e32 v108, v108
	v_pk_fma_f32 v[114:115], s[90:91], v[28:29], v[114:115]
	v_exp_f32_e32 v109, v109
	v_pk_mul_f32 v[110:111], v[70:71], v[16:17] op_sel:[1,0]
	v_pk_mul_f32 v[108:109], v[30:31], v[108:109]
	v_exp_f32_e32 v110, v110
	v_pk_fma_f32 v[30:31], v[112:113], s[76:77], v[108:109] op_sel_hi:[0,1,1]
	v_exp_f32_e32 v111, v111
	v_pk_fma_f32 v[114:115], s[92:93], v[30:31], v[114:115]
	v_pk_mul_f32 v[110:111], v[32:33], v[110:111]
	v_cvt_f32_f16_sdwa v117, v80 dst_sel:DWORD dst_unused:UNUSED_PAD src0_sel:WORD_1
	v_pk_fma_f32 v[32:33], v[112:113], s[78:79], v[110:111] op_sel_hi:[0,1,1]
	s_nop 0
	v_pk_fma_f32 v[114:115], s[94:95], v[32:33], v[114:115]
	s_nop 0
	v_add_f32_e32 v116, v114, v115
	v_fmac_f32_e32 v116, v98, v113
	v_mul_f32_e32 v116, v116, v117
	v_fma_mixlo_f16 v116, v116, s30, 0
	global_store_short v99, v116, s[26:27]
	s_add_u32 s26, s26, 0x1000
	s_addc_u32 s27, s27, 0
	s_waitcnt lgkmcnt(0)
	s_load_dwordx16 s[64:79], s[24:25], 0xb80
	s_load_dwordx16 s[80:95], s[24:25], 0xbc0
	v_cvt_f32_f16_e32 v113, v77
	v_mul_f32_e32 v113, s29, v113
	v_mul_f32_e32 v112, v72, v113
	v_pk_mul_f32 v[104:105], v[72:73], v[2:3] op_sel_hi:[0,1]
	v_pk_mul_f32 v[106:107], v[72:73], v[4:5] op_sel_hi:[0,1]
	v_exp_f32_e32 v104, v104
	v_exp_f32_e32 v105, v105
	v_exp_f32_e32 v106, v106
	v_pk_mul_f32 v[104:105], v[18:19], v[104:105]
	v_exp_f32_e32 v107, v107
	v_pk_fma_f32 v[18:19], v[112:113], s[32:33], v[104:105] op_sel_hi:[0,1,1]
	v_pk_mul_f32 v[106:107], v[20:21], v[106:107]
	v_pk_fma_f32 v[114:115], s[48:49], v[18:19], 0 op_sel_hi:[1,1,0]
	v_pk_fma_f32 v[20:21], v[112:113], s[34:35], v[106:107] op_sel_hi:[0,1,1]
	v_pk_mul_f32 v[108:109], v[72:73], v[6:7] op_sel_hi:[0,1]
	v_pk_fma_f32 v[114:115], s[50:51], v[20:21], v[114:115]
	v_exp_f32_e32 v108, v108
	v_exp_f32_e32 v109, v109
	v_pk_mul_f32 v[110:111], v[72:73], v[8:9] op_sel_hi:[0,1]
	v_pk_mul_f32 v[108:109], v[22:23], v[108:109]
	v_exp_f32_e32 v110, v110
	v_pk_fma_f32 v[22:23], v[112:113], s[36:37], v[108:109] op_sel_hi:[0,1,1]
	v_exp_f32_e32 v111, v111
	v_pk_fma_f32 v[114:115], s[52:53], v[22:23], v[114:115]
	v_pk_mul_f32 v[110:111], v[24:25], v[110:111]
	v_pk_mul_f32 v[104:105], v[72:73], v[10:11] op_sel_hi:[0,1]
	v_pk_fma_f32 v[24:25], v[112:113], s[38:39], v[110:111] op_sel_hi:[0,1,1]
	v_exp_f32_e32 v104, v104
	v_pk_fma_f32 v[114:115], s[54:55], v[24:25], v[114:115]
	v_exp_f32_e32 v105, v105
	v_pk_mul_f32 v[106:107], v[72:73], v[12:13] op_sel_hi:[0,1]
	v_pk_mul_f32 v[104:105], v[26:27], v[104:105]
	v_exp_f32_e32 v106, v106
	v_pk_fma_f32 v[26:27], v[112:113], s[40:41], v[104:105] op_sel_hi:[0,1,1]
	v_exp_f32_e32 v107, v107
	v_pk_fma_f32 v[114:115], s[56:57], v[26:27], v[114:115]
	v_pk_mul_f32 v[106:107], v[28:29], v[106:107]
	v_pk_mul_f32 v[108:109], v[72:73], v[14:15] op_sel_hi:[0,1]
	v_pk_fma_f32 v[28:29], v[112:113], s[42:43], v[106:107] op_sel_hi:[0,1,1]
	v_exp_f32_e32 v108, v108
	v_pk_fma_f32 v[114:115], s[58:59], v[28:29], v[114:115]
	v_exp_f32_e32 v109, v109
	v_pk_mul_f32 v[110:111], v[72:73], v[16:17] op_sel_hi:[0,1]
	v_pk_mul_f32 v[108:109], v[30:31], v[108:109]
	v_exp_f32_e32 v110, v110
	v_pk_fma_f32 v[30:31], v[112:113], s[44:45], v[108:109] op_sel_hi:[0,1,1]
	v_exp_f32_e32 v111, v111
	v_pk_fma_f32 v[114:115], s[60:61], v[30:31], v[114:115]
	v_pk_mul_f32 v[110:111], v[32:33], v[110:111]
	v_cvt_f32_f16_e32 v117, v81
	v_pk_fma_f32 v[32:33], v[112:113], s[46:47], v[110:111] op_sel_hi:[0,1,1]
	s_nop 0
	v_pk_fma_f32 v[114:115], s[62:63], v[32:33], v[114:115]
	s_nop 0
	v_add_f32_e32 v116, v114, v115
	v_fmac_f32_e32 v116, v98, v113
	v_mul_f32_e32 v116, v116, v117
	v_fma_mixlo_f16 v116, v116, s30, 0
	global_store_short v99, v116, s[26:27]
	s_add_u32 s26, s26, 0x1000
	s_addc_u32 s27, s27, 0
	s_waitcnt lgkmcnt(0)
	s_load_dwordx16 s[32:47], s[24:25], 0xc00
	s_load_dwordx16 s[48:63], s[24:25], 0xc40
	v_cvt_f32_f16_sdwa v113, v77 dst_sel:DWORD dst_unused:UNUSED_PAD src0_sel:WORD_1
	s_nop 0
	v_mul_f32_e32 v113, s29, v113
	v_mul_f32_e32 v112, v73, v113
	v_pk_mul_f32 v[104:105], v[72:73], v[2:3] op_sel:[1,0]
	v_pk_mul_f32 v[106:107], v[72:73], v[4:5] op_sel:[1,0]
	v_exp_f32_e32 v104, v104
	v_exp_f32_e32 v105, v105
	v_exp_f32_e32 v106, v106
	v_pk_mul_f32 v[104:105], v[18:19], v[104:105]
	v_exp_f32_e32 v107, v107
	v_pk_fma_f32 v[18:19], v[112:113], s[64:65], v[104:105] op_sel_hi:[0,1,1]
	v_pk_mul_f32 v[106:107], v[20:21], v[106:107]
	v_pk_fma_f32 v[114:115], s[80:81], v[18:19], 0 op_sel_hi:[1,1,0]
	v_pk_fma_f32 v[20:21], v[112:113], s[66:67], v[106:107] op_sel_hi:[0,1,1]
	v_pk_mul_f32 v[108:109], v[72:73], v[6:7] op_sel:[1,0]
	v_pk_fma_f32 v[114:115], s[82:83], v[20:21], v[114:115]
	v_exp_f32_e32 v108, v108
	v_exp_f32_e32 v109, v109
	v_pk_mul_f32 v[110:111], v[72:73], v[8:9] op_sel:[1,0]
	v_pk_mul_f32 v[108:109], v[22:23], v[108:109]
	v_exp_f32_e32 v110, v110
	v_pk_fma_f32 v[22:23], v[112:113], s[68:69], v[108:109] op_sel_hi:[0,1,1]
	v_exp_f32_e32 v111, v111
	v_pk_fma_f32 v[114:115], s[84:85], v[22:23], v[114:115]
	v_pk_mul_f32 v[110:111], v[24:25], v[110:111]
	v_pk_mul_f32 v[104:105], v[72:73], v[10:11] op_sel:[1,0]
	v_pk_fma_f32 v[24:25], v[112:113], s[70:71], v[110:111] op_sel_hi:[0,1,1]
	v_exp_f32_e32 v104, v104
	v_pk_fma_f32 v[114:115], s[86:87], v[24:25], v[114:115]
	v_exp_f32_e32 v105, v105
	v_pk_mul_f32 v[106:107], v[72:73], v[12:13] op_sel:[1,0]
	v_pk_mul_f32 v[104:105], v[26:27], v[104:105]
	v_exp_f32_e32 v106, v106
	v_pk_fma_f32 v[26:27], v[112:113], s[72:73], v[104:105] op_sel_hi:[0,1,1]
	v_exp_f32_e32 v107, v107
	v_pk_fma_f32 v[114:115], s[88:89], v[26:27], v[114:115]
	v_pk_mul_f32 v[106:107], v[28:29], v[106:107]
	v_pk_mul_f32 v[108:109], v[72:73], v[14:15] op_sel:[1,0]
	v_pk_fma_f32 v[28:29], v[112:113], s[74:75], v[106:107] op_sel_hi:[0,1,1]
	v_exp_f32_e32 v108, v108
	v_pk_fma_f32 v[114:115], s[90:91], v[28:29], v[114:115]
	v_exp_f32_e32 v109, v109
	v_pk_mul_f32 v[110:111], v[72:73], v[16:17] op_sel:[1,0]
	v_pk_mul_f32 v[108:109], v[30:31], v[108:109]
	v_exp_f32_e32 v110, v110
	v_pk_fma_f32 v[30:31], v[112:113], s[76:77], v[108:109] op_sel_hi:[0,1,1]
	v_exp_f32_e32 v111, v111
	v_pk_fma_f32 v[114:115], s[92:93], v[30:31], v[114:115]
	v_pk_mul_f32 v[110:111], v[32:33], v[110:111]
	v_cvt_f32_f16_sdwa v117, v81 dst_sel:DWORD dst_unused:UNUSED_PAD src0_sel:WORD_1
	v_pk_fma_f32 v[32:33], v[112:113], s[78:79], v[110:111] op_sel_hi:[0,1,1]
	s_nop 0
	v_pk_fma_f32 v[114:115], s[94:95], v[32:33], v[114:115]
	s_nop 0
	v_add_f32_e32 v116, v114, v115
	v_fmac_f32_e32 v116, v98, v113
	v_mul_f32_e32 v116, v116, v117
	v_fma_mixlo_f16 v116, v116, s30, 0
	global_store_short v99, v116, s[26:27]
	s_add_u32 s26, s26, 0x1000
	s_addc_u32 s27, s27, 0
	s_waitcnt vmcnt(16)
	s_waitcnt lgkmcnt(0)
	s_load_dwordx16 s[64:79], s[24:25], 0xc80
	s_load_dwordx16 s[80:95], s[24:25], 0xcc0
	v_cvt_f32_f16_e32 v113, v90
	v_mul_f32_e32 v113, s29, v113
	v_mul_f32_e32 v112, v82, v113
	v_pk_mul_f32 v[104:105], v[82:83], v[2:3] op_sel_hi:[0,1]
	v_pk_mul_f32 v[106:107], v[82:83], v[4:5] op_sel_hi:[0,1]
	v_exp_f32_e32 v104, v104
	v_exp_f32_e32 v105, v105
	v_exp_f32_e32 v106, v106
	v_pk_mul_f32 v[104:105], v[18:19], v[104:105]
	v_exp_f32_e32 v107, v107
	v_pk_fma_f32 v[18:19], v[112:113], s[32:33], v[104:105] op_sel_hi:[0,1,1]
	v_pk_mul_f32 v[106:107], v[20:21], v[106:107]
	v_pk_fma_f32 v[114:115], s[48:49], v[18:19], 0 op_sel_hi:[1,1,0]
	v_pk_fma_f32 v[20:21], v[112:113], s[34:35], v[106:107] op_sel_hi:[0,1,1]
	v_pk_mul_f32 v[108:109], v[82:83], v[6:7] op_sel_hi:[0,1]
	v_pk_fma_f32 v[114:115], s[50:51], v[20:21], v[114:115]
	v_exp_f32_e32 v108, v108
	v_exp_f32_e32 v109, v109
	v_pk_mul_f32 v[110:111], v[82:83], v[8:9] op_sel_hi:[0,1]
	v_pk_mul_f32 v[108:109], v[22:23], v[108:109]
	v_exp_f32_e32 v110, v110
	v_pk_fma_f32 v[22:23], v[112:113], s[36:37], v[108:109] op_sel_hi:[0,1,1]
	v_exp_f32_e32 v111, v111
	v_pk_fma_f32 v[114:115], s[52:53], v[22:23], v[114:115]
	v_pk_mul_f32 v[110:111], v[24:25], v[110:111]
	v_pk_mul_f32 v[104:105], v[82:83], v[10:11] op_sel_hi:[0,1]
	v_pk_fma_f32 v[24:25], v[112:113], s[38:39], v[110:111] op_sel_hi:[0,1,1]
	v_exp_f32_e32 v104, v104
	v_pk_fma_f32 v[114:115], s[54:55], v[24:25], v[114:115]
	v_exp_f32_e32 v105, v105
	v_pk_mul_f32 v[106:107], v[82:83], v[12:13] op_sel_hi:[0,1]
	v_pk_mul_f32 v[104:105], v[26:27], v[104:105]
	v_exp_f32_e32 v106, v106
	v_pk_fma_f32 v[26:27], v[112:113], s[40:41], v[104:105] op_sel_hi:[0,1,1]
	v_exp_f32_e32 v107, v107
	v_pk_fma_f32 v[114:115], s[56:57], v[26:27], v[114:115]
	v_pk_mul_f32 v[106:107], v[28:29], v[106:107]
	v_pk_mul_f32 v[108:109], v[82:83], v[14:15] op_sel_hi:[0,1]
	v_pk_fma_f32 v[28:29], v[112:113], s[42:43], v[106:107] op_sel_hi:[0,1,1]
	v_exp_f32_e32 v108, v108
	v_pk_fma_f32 v[114:115], s[58:59], v[28:29], v[114:115]
	v_exp_f32_e32 v109, v109
	v_pk_mul_f32 v[110:111], v[82:83], v[16:17] op_sel_hi:[0,1]
	v_pk_mul_f32 v[108:109], v[30:31], v[108:109]
	v_exp_f32_e32 v110, v110
	v_pk_fma_f32 v[30:31], v[112:113], s[44:45], v[108:109] op_sel_hi:[0,1,1]
	v_exp_f32_e32 v111, v111
	v_pk_fma_f32 v[114:115], s[60:61], v[30:31], v[114:115]
	v_pk_mul_f32 v[110:111], v[32:33], v[110:111]
	v_cvt_f32_f16_e32 v117, v94
	v_pk_fma_f32 v[32:33], v[112:113], s[46:47], v[110:111] op_sel_hi:[0,1,1]
	s_nop 0
	v_pk_fma_f32 v[114:115], s[62:63], v[32:33], v[114:115]
	s_nop 0
	v_add_f32_e32 v116, v114, v115
	v_fmac_f32_e32 v116, v98, v113
	v_mul_f32_e32 v116, v116, v117
	v_fma_mixlo_f16 v116, v116, s30, 0
	global_store_short v99, v116, s[26:27]
	s_add_u32 s26, s26, 0x1000
	s_addc_u32 s27, s27, 0
	s_waitcnt lgkmcnt(0)
	s_load_dwordx16 s[32:47], s[24:25], 0xd00
	s_load_dwordx16 s[48:63], s[24:25], 0xd40
	v_cvt_f32_f16_sdwa v113, v90 dst_sel:DWORD dst_unused:UNUSED_PAD src0_sel:WORD_1
	s_nop 0
	v_mul_f32_e32 v113, s29, v113
	v_mul_f32_e32 v112, v83, v113
	v_pk_mul_f32 v[104:105], v[82:83], v[2:3] op_sel:[1,0]
	v_pk_mul_f32 v[106:107], v[82:83], v[4:5] op_sel:[1,0]
	v_exp_f32_e32 v104, v104
	v_exp_f32_e32 v105, v105
	v_exp_f32_e32 v106, v106
	v_pk_mul_f32 v[104:105], v[18:19], v[104:105]
	v_exp_f32_e32 v107, v107
	v_pk_fma_f32 v[18:19], v[112:113], s[64:65], v[104:105] op_sel_hi:[0,1,1]
	v_pk_mul_f32 v[106:107], v[20:21], v[106:107]
	v_pk_fma_f32 v[114:115], s[80:81], v[18:19], 0 op_sel_hi:[1,1,0]
	v_pk_fma_f32 v[20:21], v[112:113], s[66:67], v[106:107] op_sel_hi:[0,1,1]
	v_pk_mul_f32 v[108:109], v[82:83], v[6:7] op_sel:[1,0]
	v_pk_fma_f32 v[114:115], s[82:83], v[20:21], v[114:115]
	v_exp_f32_e32 v108, v108
	v_exp_f32_e32 v109, v109
	v_pk_mul_f32 v[110:111], v[82:83], v[8:9] op_sel:[1,0]
	v_pk_mul_f32 v[108:109], v[22:23], v[108:109]
	v_exp_f32_e32 v110, v110
	v_pk_fma_f32 v[22:23], v[112:113], s[68:69], v[108:109] op_sel_hi:[0,1,1]
	v_exp_f32_e32 v111, v111
	v_pk_fma_f32 v[114:115], s[84:85], v[22:23], v[114:115]
	v_pk_mul_f32 v[110:111], v[24:25], v[110:111]
	v_pk_mul_f32 v[104:105], v[82:83], v[10:11] op_sel:[1,0]
	v_pk_fma_f32 v[24:25], v[112:113], s[70:71], v[110:111] op_sel_hi:[0,1,1]
	v_exp_f32_e32 v104, v104
	v_pk_fma_f32 v[114:115], s[86:87], v[24:25], v[114:115]
	v_exp_f32_e32 v105, v105
	v_pk_mul_f32 v[106:107], v[82:83], v[12:13] op_sel:[1,0]
	v_pk_mul_f32 v[104:105], v[26:27], v[104:105]
	v_exp_f32_e32 v106, v106
	v_pk_fma_f32 v[26:27], v[112:113], s[72:73], v[104:105] op_sel_hi:[0,1,1]
	v_exp_f32_e32 v107, v107
	v_pk_fma_f32 v[114:115], s[88:89], v[26:27], v[114:115]
	v_pk_mul_f32 v[106:107], v[28:29], v[106:107]
	v_pk_mul_f32 v[108:109], v[82:83], v[14:15] op_sel:[1,0]
	v_pk_fma_f32 v[28:29], v[112:113], s[74:75], v[106:107] op_sel_hi:[0,1,1]
	v_exp_f32_e32 v108, v108
	v_pk_fma_f32 v[114:115], s[90:91], v[28:29], v[114:115]
	v_exp_f32_e32 v109, v109
	v_pk_mul_f32 v[110:111], v[82:83], v[16:17] op_sel:[1,0]
	v_pk_mul_f32 v[108:109], v[30:31], v[108:109]
	v_exp_f32_e32 v110, v110
	v_pk_fma_f32 v[30:31], v[112:113], s[76:77], v[108:109] op_sel_hi:[0,1,1]
	v_exp_f32_e32 v111, v111
	v_pk_fma_f32 v[114:115], s[92:93], v[30:31], v[114:115]
	v_pk_mul_f32 v[110:111], v[32:33], v[110:111]
	v_cvt_f32_f16_sdwa v117, v94 dst_sel:DWORD dst_unused:UNUSED_PAD src0_sel:WORD_1
	v_pk_fma_f32 v[32:33], v[112:113], s[78:79], v[110:111] op_sel_hi:[0,1,1]
	s_nop 0
	v_pk_fma_f32 v[114:115], s[94:95], v[32:33], v[114:115]
	s_nop 0
	v_add_f32_e32 v116, v114, v115
	v_fmac_f32_e32 v116, v98, v113
	v_mul_f32_e32 v116, v116, v117
	v_fma_mixlo_f16 v116, v116, s30, 0
	global_store_short v99, v116, s[26:27]
	s_add_u32 s26, s26, 0x1000
	s_addc_u32 s27, s27, 0
	s_waitcnt lgkmcnt(0)
	s_load_dwordx16 s[64:79], s[24:25], 0xd80
	s_load_dwordx16 s[80:95], s[24:25], 0xdc0
	v_cvt_f32_f16_e32 v113, v91
	v_mul_f32_e32 v113, s29, v113
	v_mul_f32_e32 v112, v84, v113
	v_pk_mul_f32 v[104:105], v[84:85], v[2:3] op_sel_hi:[0,1]
	v_pk_mul_f32 v[106:107], v[84:85], v[4:5] op_sel_hi:[0,1]
	v_exp_f32_e32 v104, v104
	v_exp_f32_e32 v105, v105
	v_exp_f32_e32 v106, v106
	v_pk_mul_f32 v[104:105], v[18:19], v[104:105]
	v_exp_f32_e32 v107, v107
	v_pk_fma_f32 v[18:19], v[112:113], s[32:33], v[104:105] op_sel_hi:[0,1,1]
	v_pk_mul_f32 v[106:107], v[20:21], v[106:107]
	v_pk_fma_f32 v[114:115], s[48:49], v[18:19], 0 op_sel_hi:[1,1,0]
	v_pk_fma_f32 v[20:21], v[112:113], s[34:35], v[106:107] op_sel_hi:[0,1,1]
	v_pk_mul_f32 v[108:109], v[84:85], v[6:7] op_sel_hi:[0,1]
	v_pk_fma_f32 v[114:115], s[50:51], v[20:21], v[114:115]
	v_exp_f32_e32 v108, v108
	v_exp_f32_e32 v109, v109
	v_pk_mul_f32 v[110:111], v[84:85], v[8:9] op_sel_hi:[0,1]
	v_pk_mul_f32 v[108:109], v[22:23], v[108:109]
	v_exp_f32_e32 v110, v110
	v_pk_fma_f32 v[22:23], v[112:113], s[36:37], v[108:109] op_sel_hi:[0,1,1]
	v_exp_f32_e32 v111, v111
	v_pk_fma_f32 v[114:115], s[52:53], v[22:23], v[114:115]
	v_pk_mul_f32 v[110:111], v[24:25], v[110:111]
	v_pk_mul_f32 v[104:105], v[84:85], v[10:11] op_sel_hi:[0,1]
	v_pk_fma_f32 v[24:25], v[112:113], s[38:39], v[110:111] op_sel_hi:[0,1,1]
	v_exp_f32_e32 v104, v104
	v_pk_fma_f32 v[114:115], s[54:55], v[24:25], v[114:115]
	v_exp_f32_e32 v105, v105
	v_pk_mul_f32 v[106:107], v[84:85], v[12:13] op_sel_hi:[0,1]
	v_pk_mul_f32 v[104:105], v[26:27], v[104:105]
	v_exp_f32_e32 v106, v106
	v_pk_fma_f32 v[26:27], v[112:113], s[40:41], v[104:105] op_sel_hi:[0,1,1]
	v_exp_f32_e32 v107, v107
	v_pk_fma_f32 v[114:115], s[56:57], v[26:27], v[114:115]
	v_pk_mul_f32 v[106:107], v[28:29], v[106:107]
	v_pk_mul_f32 v[108:109], v[84:85], v[14:15] op_sel_hi:[0,1]
	v_pk_fma_f32 v[28:29], v[112:113], s[42:43], v[106:107] op_sel_hi:[0,1,1]
	v_exp_f32_e32 v108, v108
	v_pk_fma_f32 v[114:115], s[58:59], v[28:29], v[114:115]
	v_exp_f32_e32 v109, v109
	v_pk_mul_f32 v[110:111], v[84:85], v[16:17] op_sel_hi:[0,1]
	v_pk_mul_f32 v[108:109], v[30:31], v[108:109]
	v_exp_f32_e32 v110, v110
	v_pk_fma_f32 v[30:31], v[112:113], s[44:45], v[108:109] op_sel_hi:[0,1,1]
	v_exp_f32_e32 v111, v111
	v_pk_fma_f32 v[114:115], s[60:61], v[30:31], v[114:115]
	v_pk_mul_f32 v[110:111], v[32:33], v[110:111]
	v_cvt_f32_f16_e32 v117, v95
	v_pk_fma_f32 v[32:33], v[112:113], s[46:47], v[110:111] op_sel_hi:[0,1,1]
	s_nop 0
	v_pk_fma_f32 v[114:115], s[62:63], v[32:33], v[114:115]
	s_nop 0
	v_add_f32_e32 v116, v114, v115
	v_fmac_f32_e32 v116, v98, v113
	v_mul_f32_e32 v116, v116, v117
	v_fma_mixlo_f16 v116, v116, s30, 0
	global_store_short v99, v116, s[26:27]
	s_add_u32 s26, s26, 0x1000
	s_addc_u32 s27, s27, 0
	s_waitcnt lgkmcnt(0)
	s_load_dwordx16 s[32:47], s[24:25], 0xe00
	s_load_dwordx16 s[48:63], s[24:25], 0xe40
	v_cvt_f32_f16_sdwa v113, v91 dst_sel:DWORD dst_unused:UNUSED_PAD src0_sel:WORD_1
	s_nop 0
	v_mul_f32_e32 v113, s29, v113
	v_mul_f32_e32 v112, v85, v113
	v_pk_mul_f32 v[104:105], v[84:85], v[2:3] op_sel:[1,0]
	v_pk_mul_f32 v[106:107], v[84:85], v[4:5] op_sel:[1,0]
	v_exp_f32_e32 v104, v104
	v_exp_f32_e32 v105, v105
	v_exp_f32_e32 v106, v106
	v_pk_mul_f32 v[104:105], v[18:19], v[104:105]
	v_exp_f32_e32 v107, v107
	v_pk_fma_f32 v[18:19], v[112:113], s[64:65], v[104:105] op_sel_hi:[0,1,1]
	v_pk_mul_f32 v[106:107], v[20:21], v[106:107]
	v_pk_fma_f32 v[114:115], s[80:81], v[18:19], 0 op_sel_hi:[1,1,0]
	v_pk_fma_f32 v[20:21], v[112:113], s[66:67], v[106:107] op_sel_hi:[0,1,1]
	v_pk_mul_f32 v[108:109], v[84:85], v[6:7] op_sel:[1,0]
	v_pk_fma_f32 v[114:115], s[82:83], v[20:21], v[114:115]
	v_exp_f32_e32 v108, v108
	v_exp_f32_e32 v109, v109
	v_pk_mul_f32 v[110:111], v[84:85], v[8:9] op_sel:[1,0]
	v_pk_mul_f32 v[108:109], v[22:23], v[108:109]
	v_exp_f32_e32 v110, v110
	v_pk_fma_f32 v[22:23], v[112:113], s[68:69], v[108:109] op_sel_hi:[0,1,1]
	v_exp_f32_e32 v111, v111
	v_pk_fma_f32 v[114:115], s[84:85], v[22:23], v[114:115]
	v_pk_mul_f32 v[110:111], v[24:25], v[110:111]
	v_pk_mul_f32 v[104:105], v[84:85], v[10:11] op_sel:[1,0]
	v_pk_fma_f32 v[24:25], v[112:113], s[70:71], v[110:111] op_sel_hi:[0,1,1]
	v_exp_f32_e32 v104, v104
	v_pk_fma_f32 v[114:115], s[86:87], v[24:25], v[114:115]
	v_exp_f32_e32 v105, v105
	v_pk_mul_f32 v[106:107], v[84:85], v[12:13] op_sel:[1,0]
	v_pk_mul_f32 v[104:105], v[26:27], v[104:105]
	v_exp_f32_e32 v106, v106
	v_pk_fma_f32 v[26:27], v[112:113], s[72:73], v[104:105] op_sel_hi:[0,1,1]
	v_exp_f32_e32 v107, v107
	v_pk_fma_f32 v[114:115], s[88:89], v[26:27], v[114:115]
	v_pk_mul_f32 v[106:107], v[28:29], v[106:107]
	v_pk_mul_f32 v[108:109], v[84:85], v[14:15] op_sel:[1,0]
	v_pk_fma_f32 v[28:29], v[112:113], s[74:75], v[106:107] op_sel_hi:[0,1,1]
	v_exp_f32_e32 v108, v108
	v_pk_fma_f32 v[114:115], s[90:91], v[28:29], v[114:115]
	v_exp_f32_e32 v109, v109
	v_pk_mul_f32 v[110:111], v[84:85], v[16:17] op_sel:[1,0]
	v_pk_mul_f32 v[108:109], v[30:31], v[108:109]
	v_exp_f32_e32 v110, v110
	v_pk_fma_f32 v[30:31], v[112:113], s[76:77], v[108:109] op_sel_hi:[0,1,1]
	v_exp_f32_e32 v111, v111
	v_pk_fma_f32 v[114:115], s[92:93], v[30:31], v[114:115]
	v_pk_mul_f32 v[110:111], v[32:33], v[110:111]
	v_cvt_f32_f16_sdwa v117, v95 dst_sel:DWORD dst_unused:UNUSED_PAD src0_sel:WORD_1
	v_pk_fma_f32 v[32:33], v[112:113], s[78:79], v[110:111] op_sel_hi:[0,1,1]
	s_nop 0
	v_pk_fma_f32 v[114:115], s[94:95], v[32:33], v[114:115]
	s_nop 0
	v_add_f32_e32 v116, v114, v115
	v_fmac_f32_e32 v116, v98, v113
	v_mul_f32_e32 v116, v116, v117
	v_fma_mixlo_f16 v116, v116, s30, 0
	global_store_short v99, v116, s[26:27]
	s_add_u32 s26, s26, 0x1000
	s_addc_u32 s27, s27, 0
	s_waitcnt lgkmcnt(0)
	s_load_dwordx16 s[64:79], s[24:25], 0xe80
	s_load_dwordx16 s[80:95], s[24:25], 0xec0
	v_cvt_f32_f16_e32 v113, v92
	v_mul_f32_e32 v113, s29, v113
	v_mul_f32_e32 v112, v86, v113
	v_pk_mul_f32 v[104:105], v[86:87], v[2:3] op_sel_hi:[0,1]
	v_pk_mul_f32 v[106:107], v[86:87], v[4:5] op_sel_hi:[0,1]
	v_exp_f32_e32 v104, v104
	v_exp_f32_e32 v105, v105
	v_exp_f32_e32 v106, v106
	v_pk_mul_f32 v[104:105], v[18:19], v[104:105]
	v_exp_f32_e32 v107, v107
	v_pk_fma_f32 v[18:19], v[112:113], s[32:33], v[104:105] op_sel_hi:[0,1,1]
	v_pk_mul_f32 v[106:107], v[20:21], v[106:107]
	v_pk_fma_f32 v[114:115], s[48:49], v[18:19], 0 op_sel_hi:[1,1,0]
	v_pk_fma_f32 v[20:21], v[112:113], s[34:35], v[106:107] op_sel_hi:[0,1,1]
	v_pk_mul_f32 v[108:109], v[86:87], v[6:7] op_sel_hi:[0,1]
	v_pk_fma_f32 v[114:115], s[50:51], v[20:21], v[114:115]
	v_exp_f32_e32 v108, v108
	v_exp_f32_e32 v109, v109
	v_pk_mul_f32 v[110:111], v[86:87], v[8:9] op_sel_hi:[0,1]
	v_pk_mul_f32 v[108:109], v[22:23], v[108:109]
	v_exp_f32_e32 v110, v110
	v_pk_fma_f32 v[22:23], v[112:113], s[36:37], v[108:109] op_sel_hi:[0,1,1]
	v_exp_f32_e32 v111, v111
	v_pk_fma_f32 v[114:115], s[52:53], v[22:23], v[114:115]
	v_pk_mul_f32 v[110:111], v[24:25], v[110:111]
	v_pk_mul_f32 v[104:105], v[86:87], v[10:11] op_sel_hi:[0,1]
	v_pk_fma_f32 v[24:25], v[112:113], s[38:39], v[110:111] op_sel_hi:[0,1,1]
	v_exp_f32_e32 v104, v104
	v_pk_fma_f32 v[114:115], s[54:55], v[24:25], v[114:115]
	v_exp_f32_e32 v105, v105
	v_pk_mul_f32 v[106:107], v[86:87], v[12:13] op_sel_hi:[0,1]
	v_pk_mul_f32 v[104:105], v[26:27], v[104:105]
	v_exp_f32_e32 v106, v106
	v_pk_fma_f32 v[26:27], v[112:113], s[40:41], v[104:105] op_sel_hi:[0,1,1]
	v_exp_f32_e32 v107, v107
	v_pk_fma_f32 v[114:115], s[56:57], v[26:27], v[114:115]
	v_pk_mul_f32 v[106:107], v[28:29], v[106:107]
	v_pk_mul_f32 v[108:109], v[86:87], v[14:15] op_sel_hi:[0,1]
	v_pk_fma_f32 v[28:29], v[112:113], s[42:43], v[106:107] op_sel_hi:[0,1,1]
	v_exp_f32_e32 v108, v108
	v_pk_fma_f32 v[114:115], s[58:59], v[28:29], v[114:115]
	v_exp_f32_e32 v109, v109
	v_pk_mul_f32 v[110:111], v[86:87], v[16:17] op_sel_hi:[0,1]
	v_pk_mul_f32 v[108:109], v[30:31], v[108:109]
	v_exp_f32_e32 v110, v110
	v_pk_fma_f32 v[30:31], v[112:113], s[44:45], v[108:109] op_sel_hi:[0,1,1]
	v_exp_f32_e32 v111, v111
	v_pk_fma_f32 v[114:115], s[60:61], v[30:31], v[114:115]
	v_pk_mul_f32 v[110:111], v[32:33], v[110:111]
	v_cvt_f32_f16_e32 v117, v96
	v_pk_fma_f32 v[32:33], v[112:113], s[46:47], v[110:111] op_sel_hi:[0,1,1]
	s_nop 0
	v_pk_fma_f32 v[114:115], s[62:63], v[32:33], v[114:115]
	s_nop 0
	v_add_f32_e32 v116, v114, v115
	v_fmac_f32_e32 v116, v98, v113
	v_mul_f32_e32 v116, v116, v117
	v_fma_mixlo_f16 v116, v116, s30, 0
	global_store_short v99, v116, s[26:27]
	s_add_u32 s26, s26, 0x1000
	s_addc_u32 s27, s27, 0
	s_waitcnt lgkmcnt(0)
	s_load_dwordx16 s[32:47], s[24:25], 0xf00
	s_load_dwordx16 s[48:63], s[24:25], 0xf40
	v_cvt_f32_f16_sdwa v113, v92 dst_sel:DWORD dst_unused:UNUSED_PAD src0_sel:WORD_1
	s_nop 0
	v_mul_f32_e32 v113, s29, v113
	v_mul_f32_e32 v112, v87, v113
	v_pk_mul_f32 v[104:105], v[86:87], v[2:3] op_sel:[1,0]
	v_pk_mul_f32 v[106:107], v[86:87], v[4:5] op_sel:[1,0]
	v_exp_f32_e32 v104, v104
	v_exp_f32_e32 v105, v105
	v_exp_f32_e32 v106, v106
	v_pk_mul_f32 v[104:105], v[18:19], v[104:105]
	v_exp_f32_e32 v107, v107
	v_pk_fma_f32 v[18:19], v[112:113], s[64:65], v[104:105] op_sel_hi:[0,1,1]
	v_pk_mul_f32 v[106:107], v[20:21], v[106:107]
	v_pk_fma_f32 v[114:115], s[80:81], v[18:19], 0 op_sel_hi:[1,1,0]
	v_pk_fma_f32 v[20:21], v[112:113], s[66:67], v[106:107] op_sel_hi:[0,1,1]
	v_pk_mul_f32 v[108:109], v[86:87], v[6:7] op_sel:[1,0]
	v_pk_fma_f32 v[114:115], s[82:83], v[20:21], v[114:115]
	v_exp_f32_e32 v108, v108
	v_exp_f32_e32 v109, v109
	v_pk_mul_f32 v[110:111], v[86:87], v[8:9] op_sel:[1,0]
	v_pk_mul_f32 v[108:109], v[22:23], v[108:109]
	v_exp_f32_e32 v110, v110
	v_pk_fma_f32 v[22:23], v[112:113], s[68:69], v[108:109] op_sel_hi:[0,1,1]
	v_exp_f32_e32 v111, v111
	v_pk_fma_f32 v[114:115], s[84:85], v[22:23], v[114:115]
	v_pk_mul_f32 v[110:111], v[24:25], v[110:111]
	v_pk_mul_f32 v[104:105], v[86:87], v[10:11] op_sel:[1,0]
	v_pk_fma_f32 v[24:25], v[112:113], s[70:71], v[110:111] op_sel_hi:[0,1,1]
	v_exp_f32_e32 v104, v104
	v_pk_fma_f32 v[114:115], s[86:87], v[24:25], v[114:115]
	v_exp_f32_e32 v105, v105
	v_pk_mul_f32 v[106:107], v[86:87], v[12:13] op_sel:[1,0]
	v_pk_mul_f32 v[104:105], v[26:27], v[104:105]
	v_exp_f32_e32 v106, v106
	v_pk_fma_f32 v[26:27], v[112:113], s[72:73], v[104:105] op_sel_hi:[0,1,1]
	v_exp_f32_e32 v107, v107
	v_pk_fma_f32 v[114:115], s[88:89], v[26:27], v[114:115]
	v_pk_mul_f32 v[106:107], v[28:29], v[106:107]
	v_pk_mul_f32 v[108:109], v[86:87], v[14:15] op_sel:[1,0]
	v_pk_fma_f32 v[28:29], v[112:113], s[74:75], v[106:107] op_sel_hi:[0,1,1]
	v_exp_f32_e32 v108, v108
	v_pk_fma_f32 v[114:115], s[90:91], v[28:29], v[114:115]
	v_exp_f32_e32 v109, v109
	v_pk_mul_f32 v[110:111], v[86:87], v[16:17] op_sel:[1,0]
	v_pk_mul_f32 v[108:109], v[30:31], v[108:109]
	v_exp_f32_e32 v110, v110
	v_pk_fma_f32 v[30:31], v[112:113], s[76:77], v[108:109] op_sel_hi:[0,1,1]
	v_exp_f32_e32 v111, v111
	v_pk_fma_f32 v[114:115], s[92:93], v[30:31], v[114:115]
	v_pk_mul_f32 v[110:111], v[32:33], v[110:111]
	v_cvt_f32_f16_sdwa v117, v96 dst_sel:DWORD dst_unused:UNUSED_PAD src0_sel:WORD_1
	v_pk_fma_f32 v[32:33], v[112:113], s[78:79], v[110:111] op_sel_hi:[0,1,1]
	s_nop 0
	v_pk_fma_f32 v[114:115], s[94:95], v[32:33], v[114:115]
	s_nop 0
	v_add_f32_e32 v116, v114, v115
	v_fmac_f32_e32 v116, v98, v113
	v_mul_f32_e32 v116, v116, v117
	v_fma_mixlo_f16 v116, v116, s30, 0
	global_store_short v99, v116, s[26:27]
	s_add_u32 s26, s26, 0x1000
	s_addc_u32 s27, s27, 0
	s_waitcnt lgkmcnt(0)
	s_load_dwordx16 s[64:79], s[24:25], 0xf80
	s_load_dwordx16 s[80:95], s[24:25], 0xfc0
	v_cvt_f32_f16_e32 v113, v93
	v_mul_f32_e32 v113, s29, v113
	v_mul_f32_e32 v112, v88, v113
	v_pk_mul_f32 v[104:105], v[88:89], v[2:3] op_sel_hi:[0,1]
	v_pk_mul_f32 v[106:107], v[88:89], v[4:5] op_sel_hi:[0,1]
	v_exp_f32_e32 v104, v104
	v_exp_f32_e32 v105, v105
	v_exp_f32_e32 v106, v106
	v_pk_mul_f32 v[104:105], v[18:19], v[104:105]
	v_exp_f32_e32 v107, v107
	v_pk_fma_f32 v[18:19], v[112:113], s[32:33], v[104:105] op_sel_hi:[0,1,1]
	v_pk_mul_f32 v[106:107], v[20:21], v[106:107]
	v_pk_fma_f32 v[114:115], s[48:49], v[18:19], 0 op_sel_hi:[1,1,0]
	v_pk_fma_f32 v[20:21], v[112:113], s[34:35], v[106:107] op_sel_hi:[0,1,1]
	v_pk_mul_f32 v[108:109], v[88:89], v[6:7] op_sel_hi:[0,1]
	v_pk_fma_f32 v[114:115], s[50:51], v[20:21], v[114:115]
	v_exp_f32_e32 v108, v108
	v_exp_f32_e32 v109, v109
	v_pk_mul_f32 v[110:111], v[88:89], v[8:9] op_sel_hi:[0,1]
	v_pk_mul_f32 v[108:109], v[22:23], v[108:109]
	v_exp_f32_e32 v110, v110
	v_pk_fma_f32 v[22:23], v[112:113], s[36:37], v[108:109] op_sel_hi:[0,1,1]
	v_exp_f32_e32 v111, v111
	v_pk_fma_f32 v[114:115], s[52:53], v[22:23], v[114:115]
	v_pk_mul_f32 v[110:111], v[24:25], v[110:111]
	v_pk_mul_f32 v[104:105], v[88:89], v[10:11] op_sel_hi:[0,1]
	v_pk_fma_f32 v[24:25], v[112:113], s[38:39], v[110:111] op_sel_hi:[0,1,1]
	v_exp_f32_e32 v104, v104
	v_pk_fma_f32 v[114:115], s[54:55], v[24:25], v[114:115]
	v_exp_f32_e32 v105, v105
	v_pk_mul_f32 v[106:107], v[88:89], v[12:13] op_sel_hi:[0,1]
	v_pk_mul_f32 v[104:105], v[26:27], v[104:105]
	v_exp_f32_e32 v106, v106
	v_pk_fma_f32 v[26:27], v[112:113], s[40:41], v[104:105] op_sel_hi:[0,1,1]
	v_exp_f32_e32 v107, v107
	v_pk_fma_f32 v[114:115], s[56:57], v[26:27], v[114:115]
	v_pk_mul_f32 v[106:107], v[28:29], v[106:107]
	v_pk_mul_f32 v[108:109], v[88:89], v[14:15] op_sel_hi:[0,1]
	v_pk_fma_f32 v[28:29], v[112:113], s[42:43], v[106:107] op_sel_hi:[0,1,1]
	v_exp_f32_e32 v108, v108
	v_pk_fma_f32 v[114:115], s[58:59], v[28:29], v[114:115]
	v_exp_f32_e32 v109, v109
	v_pk_mul_f32 v[110:111], v[88:89], v[16:17] op_sel_hi:[0,1]
	v_pk_mul_f32 v[108:109], v[30:31], v[108:109]
	v_exp_f32_e32 v110, v110
	v_pk_fma_f32 v[30:31], v[112:113], s[44:45], v[108:109] op_sel_hi:[0,1,1]
	v_exp_f32_e32 v111, v111
	v_pk_fma_f32 v[114:115], s[60:61], v[30:31], v[114:115]
	v_pk_mul_f32 v[110:111], v[32:33], v[110:111]
	v_cvt_f32_f16_e32 v117, v97
	v_pk_fma_f32 v[32:33], v[112:113], s[46:47], v[110:111] op_sel_hi:[0,1,1]
	s_nop 0
	v_pk_fma_f32 v[114:115], s[62:63], v[32:33], v[114:115]
	s_nop 0
	v_add_f32_e32 v116, v114, v115
	v_fmac_f32_e32 v116, v98, v113
	v_mul_f32_e32 v116, v116, v117
	v_fma_mixlo_f16 v116, v116, s30, 0
	global_store_short v99, v116, s[26:27]
	s_add_u32 s26, s26, 0x1000
	s_addc_u32 s27, s27, 0
	s_waitcnt lgkmcnt(0)
	v_cvt_f32_f16_sdwa v113, v93 dst_sel:DWORD dst_unused:UNUSED_PAD src0_sel:WORD_1
	s_nop 0
	v_mul_f32_e32 v113, s29, v113
	v_mul_f32_e32 v112, v89, v113
	v_pk_mul_f32 v[104:105], v[88:89], v[2:3] op_sel:[1,0]
	v_pk_mul_f32 v[106:107], v[88:89], v[4:5] op_sel:[1,0]
	v_exp_f32_e32 v104, v104
	v_exp_f32_e32 v105, v105
	v_exp_f32_e32 v106, v106
	v_pk_mul_f32 v[104:105], v[18:19], v[104:105]
	v_exp_f32_e32 v107, v107
	v_pk_fma_f32 v[18:19], v[112:113], s[64:65], v[104:105] op_sel_hi:[0,1,1]
	v_pk_mul_f32 v[106:107], v[20:21], v[106:107]
	v_pk_fma_f32 v[114:115], s[80:81], v[18:19], 0 op_sel_hi:[1,1,0]
	v_pk_fma_f32 v[20:21], v[112:113], s[66:67], v[106:107] op_sel_hi:[0,1,1]
	v_pk_mul_f32 v[108:109], v[88:89], v[6:7] op_sel:[1,0]
	v_pk_fma_f32 v[114:115], s[82:83], v[20:21], v[114:115]
	v_exp_f32_e32 v108, v108
	v_exp_f32_e32 v109, v109
	v_pk_mul_f32 v[110:111], v[88:89], v[8:9] op_sel:[1,0]
	v_pk_mul_f32 v[108:109], v[22:23], v[108:109]
	v_exp_f32_e32 v110, v110
	v_pk_fma_f32 v[22:23], v[112:113], s[68:69], v[108:109] op_sel_hi:[0,1,1]
	v_exp_f32_e32 v111, v111
	v_pk_fma_f32 v[114:115], s[84:85], v[22:23], v[114:115]
	v_pk_mul_f32 v[110:111], v[24:25], v[110:111]
	v_pk_mul_f32 v[104:105], v[88:89], v[10:11] op_sel:[1,0]
	v_pk_fma_f32 v[24:25], v[112:113], s[70:71], v[110:111] op_sel_hi:[0,1,1]
	v_exp_f32_e32 v104, v104
	v_pk_fma_f32 v[114:115], s[86:87], v[24:25], v[114:115]
	v_exp_f32_e32 v105, v105
	v_pk_mul_f32 v[106:107], v[88:89], v[12:13] op_sel:[1,0]
	v_pk_mul_f32 v[104:105], v[26:27], v[104:105]
	v_exp_f32_e32 v106, v106
	v_pk_fma_f32 v[26:27], v[112:113], s[72:73], v[104:105] op_sel_hi:[0,1,1]
	v_exp_f32_e32 v107, v107
	v_pk_fma_f32 v[114:115], s[88:89], v[26:27], v[114:115]
	v_pk_mul_f32 v[106:107], v[28:29], v[106:107]
	v_pk_mul_f32 v[108:109], v[88:89], v[14:15] op_sel:[1,0]
	v_pk_fma_f32 v[28:29], v[112:113], s[74:75], v[106:107] op_sel_hi:[0,1,1]
	v_exp_f32_e32 v108, v108
	v_pk_fma_f32 v[114:115], s[90:91], v[28:29], v[114:115]
	v_exp_f32_e32 v109, v109
	v_pk_mul_f32 v[110:111], v[88:89], v[16:17] op_sel:[1,0]
	v_pk_mul_f32 v[108:109], v[30:31], v[108:109]
	v_exp_f32_e32 v110, v110
	v_pk_fma_f32 v[30:31], v[112:113], s[76:77], v[108:109] op_sel_hi:[0,1,1]
	v_exp_f32_e32 v111, v111
	v_pk_fma_f32 v[114:115], s[92:93], v[30:31], v[114:115]
	v_pk_mul_f32 v[110:111], v[32:33], v[110:111]
	v_cvt_f32_f16_sdwa v117, v97 dst_sel:DWORD dst_unused:UNUSED_PAD src0_sel:WORD_1
	v_pk_fma_f32 v[32:33], v[112:113], s[78:79], v[110:111] op_sel_hi:[0,1,1]
	s_nop 0
	v_pk_fma_f32 v[114:115], s[94:95], v[32:33], v[114:115]
	s_nop 0
	v_add_f32_e32 v116, v114, v115
	v_fmac_f32_e32 v116, v98, v113
	v_mul_f32_e32 v116, v116, v117
	v_fma_mixlo_f16 v116, v116, s30, 0
	global_store_short v99, v116, s[26:27]
	s_endpgm
	.p2alignl 8, 3212836864

	.amdhsa_kernel _Z10scan_pass2PKDF16_PKfS2_S0_S2_S0_PDF16_S2_
		.amdhsa_group_segment_fixed_size 4096
		.amdhsa_private_segment_fixed_size 0
		.amdhsa_kernarg_size 64
		.amdhsa_user_sgpr_count 2
		.amdhsa_user_sgpr_dispatch_ptr 0
		.amdhsa_user_sgpr_queue_ptr 0
		.amdhsa_user_sgpr_kernarg_segment_ptr 1
		.amdhsa_user_sgpr_dispatch_id 0
		.amdhsa_user_sgpr_kernarg_preload_length 0
		.amdhsa_user_sgpr_kernarg_preload_offset 0
		.amdhsa_user_sgpr_private_segment_size 0
		.amdhsa_uses_dynamic_stack 0
		.amdhsa_enable_private_segment 0
		.amdhsa_system_sgpr_workgroup_id_x 1
		.amdhsa_system_sgpr_workgroup_id_y 1
		.amdhsa_system_sgpr_workgroup_id_z 1
		.amdhsa_system_sgpr_workgroup_info 0
		.amdhsa_system_vgpr_workitem_id 0
		.amdhsa_next_free_vgpr 118
		.amdhsa_next_free_sgpr 98
		.amdhsa_accum_offset 120
		.amdhsa_reserve_vcc 1
		.amdhsa_float_round_mode_32 0
		.amdhsa_float_round_mode_16_64 0
		.amdhsa_float_denorm_mode_32 3
		.amdhsa_float_denorm_mode_16_64 3
		.amdhsa_dx10_clamp 1
		.amdhsa_ieee_mode 1
		.amdhsa_fp16_overflow 0
		.amdhsa_tg_split 0
		.amdhsa_exception_fp_ieee_invalid_op 0
		.amdhsa_exception_fp_denorm_src 0
		.amdhsa_exception_fp_ieee_div_zero 0
		.amdhsa_exception_fp_ieee_overflow 0
		.amdhsa_exception_fp_ieee_underflow 0
		.amdhsa_exception_fp_ieee_inexact 0
		.amdhsa_exception_int_div_zero 0
	.end_amdhsa_kernel

amdhsa.kernels:
  - .agpr_count:     0
    .args:
      - .address_space:  global
        .offset:         0
        .size:           8
        .value_kind:     global_buffer
      - .address_space:  global
        .offset:         8
        .size:           8
        .value_kind:     global_buffer
      - .offset:         16
        .size:           8
        .value_kind:     by_value
      - .address_space:  global
        .offset:         24
        .size:           8
        .value_kind:     global_buffer
      - .address_space:  global
        .offset:         32
        .size:           8
        .value_kind:     global_buffer
      - .offset:         40
        .size:           8
        .value_kind:     by_value
      - .address_space:  global
        .offset:         48
        .size:           8
        .value_kind:     global_buffer
      - .address_space:  global
        .offset:         56
        .size:           8
        .value_kind:     global_buffer
      - .offset:         64
        .size:           8
        .value_kind:     by_value
      - .address_space:  global
        .offset:         72
        .size:           8
        .value_kind:     global_buffer
      - .address_space:  global
        .offset:         80
        .size:           8
        .value_kind:     global_buffer
      - .offset:         88
        .size:           8
        .value_kind:     by_value
      - .address_space:  global
        .offset:         96
        .size:           8
        .value_kind:     global_buffer
      - .address_space:  global
        .offset:         104
        .size:           8
        .value_kind:     global_buffer
      - .offset:         112
        .size:           8
        .value_kind:     by_value
      - .address_space:  global
        .offset:         120
        .size:           8
        .value_kind:     global_buffer
      - .actual_access:  read_only
        .address_space:  global
        .offset:         128
        .size:           8
        .value_kind:     global_buffer
      - .actual_access:  write_only
        .address_space:  global
        .offset:         136
        .size:           8
        .value_kind:     global_buffer
    .group_segment_fixed_size: 0
    .kernarg_segment_align: 8
    .kernarg_segment_size: 144
    .language:       OpenCL C
    .language_version:
      - 2
      - 0
    .max_flat_workgroup_size: 256
    .name:           _Z10cvt_kernelPKfPDF16_lS0_S1_lS0_S1_lS0_S1_lS0_S1_lPjS0_Pf
    .private_segment_fixed_size: 0
    .sgpr_count:     58
    .sgpr_spill_count: 0
    .symbol:         _Z10cvt_kernelPKfPDF16_lS0_S1_lS0_S1_lS0_S1_lS0_S1_lPjS0_Pf.kd
    .uniform_work_group_size: 1
    .uses_dynamic_stack: false
    .vgpr_count:     18
    .vgpr_spill_count: 0
    .wavefront_size: 64
  - .agpr_count:     0
    .args:
      - .actual_access:  read_only
        .address_space:  global
        .offset:         0
        .size:           8
        .value_kind:     global_buffer
      - .actual_access:  read_only
        .address_space:  global
        .offset:         8
        .size:           8
        .value_kind:     global_buffer
      - .actual_access:  read_only
        .address_space:  global
        .offset:         16
        .size:           8
        .value_kind:     global_buffer
      - .actual_access:  read_only
        .address_space:  global
        .offset:         24
        .size:           8
        .value_kind:     global_buffer
      - .actual_access:  write_only
        .address_space:  global
        .offset:         32
        .size:           8
        .value_kind:     global_buffer
      - .actual_access:  write_only
        .address_space:  global
        .offset:         40
        .size:           8
        .value_kind:     global_buffer
      - .actual_access:  write_only
        .address_space:  global
        .offset:         48
        .size:           8
        .value_kind:     global_buffer
    .group_segment_fixed_size: 65792
    .kernarg_segment_align: 8
    .kernarg_segment_size: 56
    .language:       OpenCL C
    .language_version:
      - 2
      - 0
    .max_flat_workgroup_size: 1024
    .name:           _Z17conv_xproj_kernelPKDF16_PKfS2_S0_PDF16_S3_Pf
    .private_segment_fixed_size: 0
    .sgpr_count:     22
    .sgpr_spill_count: 0
    .symbol:         _Z17conv_xproj_kernelPKDF16_PKfS2_S0_PDF16_S3_Pf.kd
    .uniform_work_group_size: 1
    .uses_dynamic_stack: false
    .vgpr_count:     126
    .vgpr_spill_count: 0
    .wavefront_size: 64
  - .agpr_count:     0
    .args:
      - .actual_access:  read_only
        .address_space:  global
        .offset:         0
        .size:           8
        .value_kind:     global_buffer
      - .actual_access:  read_only
        .address_space:  global
        .offset:         8
        .size:           8
        .value_kind:     global_buffer
      - .actual_access:  read_only
        .address_space:  global
        .offset:         16
        .size:           8
        .value_kind:     global_buffer
      - .actual_access:  read_only
        .address_space:  global
        .offset:         24
        .size:           8
        .value_kind:     global_buffer
      - .actual_access:  read_only
        .address_space:  global
        .offset:         32
        .size:           8
        .value_kind:     global_buffer
      - .actual_access:  read_only
        .address_space:  global
        .offset:         40
        .size:           8
        .value_kind:     global_buffer
      - .actual_access:  write_only
        .address_space:  global
        .offset:         48
        .size:           8
        .value_kind:     global_buffer
      - .actual_access:  write_only
        .address_space:  global
        .offset:         56
        .size:           8
        .value_kind:     global_buffer
      - .actual_access:  write_only
        .address_space:  global
        .offset:         64
        .size:           8
        .value_kind:     global_buffer
      - .actual_access:  read_only
        .address_space:  global
        .offset:         72
        .size:           8
        .value_kind:     global_buffer
      - .actual_access:  write_only
        .address_space:  global
        .offset:         80
        .size:           8
        .value_kind:     global_buffer
    .group_segment_fixed_size: 4096
    .kernarg_segment_align: 8
    .kernarg_segment_size: 88
    .language:       OpenCL C
    .language_version:
      - 2
      - 0
    .max_flat_workgroup_size: 256
    .name:           _Z10scan_pass1PKDF16_S0_PKfS0_S2_S2_PDF16_PfS4_S2_S3_
    .private_segment_fixed_size: 0
    .sgpr_count:     36
    .sgpr_spill_count: 0
    .symbol:         _Z10scan_pass1PKDF16_S0_PKfS0_S2_S2_PDF16_PfS4_S2_S3_.kd
    .uniform_work_group_size: 1
    .uses_dynamic_stack: false
    .vgpr_count:     104
    .vgpr_spill_count: 0
    .wavefront_size: 64
  - .agpr_count:     0
    .args:
      - .actual_access:  read_only
        .address_space:  global
        .offset:         0
        .size:           8
        .value_kind:     global_buffer
      - .actual_access:  read_only
        .address_space:  global
        .offset:         8
        .size:           8
        .value_kind:     global_buffer
      - .actual_access:  read_only
        .address_space:  global
        .offset:         16
        .size:           8
        .value_kind:     global_buffer
      - .actual_access:  read_only
        .address_space:  global
        .offset:         24
        .size:           8
        .value_kind:     global_buffer
      - .actual_access:  read_only
        .address_space:  global
        .offset:         32
        .size:           8
        .value_kind:     global_buffer
      - .actual_access:  read_only
        .address_space:  global
        .offset:         40
        .size:           8
        .value_kind:     global_buffer
      - .actual_access:  write_only
        .address_space:  global
        .offset:         48
        .size:           8
        .value_kind:     global_buffer
      - .actual_access:  read_only
        .address_space:  global
        .offset:         56
        .size:           8
        .value_kind:     global_buffer
    .group_segment_fixed_size: 4096
    .kernarg_segment_align: 8
    .kernarg_segment_size: 64
    .language:       OpenCL C
    .language_version:
      - 2
      - 0
    .max_flat_workgroup_size: 256
    .name:           _Z10scan_pass2PKDF16_PKfS2_S0_S2_S0_PDF16_S2_
    .private_segment_fixed_size: 0
    .sgpr_count:     104
    .sgpr_spill_count: 0
    .symbol:         _Z10scan_pass2PKDF16_PKfS2_S0_S2_S0_PDF16_S2_.kd
    .uniform_work_group_size: 1
    .uses_dynamic_stack: false
    .vgpr_count:     118
    .vgpr_spill_count: 0
    .wavefront_size: 64
  - .agpr_count:     0
    .args:
      - .actual_access:  read_only
        .address_space:  global
        .offset:         0
        .size:           8
        .value_kind:     global_buffer
      - .actual_access:  read_only
        .address_space:  global
        .offset:         8
        .size:           8
        .value_kind:     global_buffer
      - .actual_access:  read_only
        .address_space:  global
        .offset:         16
        .size:           8
        .value_kind:     global_buffer
      - .actual_access:  write_only
        .address_space:  global
        .offset:         24
        .size:           8
        .value_kind:     global_buffer
    .group_segment_fixed_size: 8192
    .kernarg_segment_align: 8
    .kernarg_segment_size: 32
    .language:       OpenCL C
    .language_version:
      - 2
      - 0
    .max_flat_workgroup_size: 512
    .name:           _Z12scan_combinePKfPKDF16_S0_PDF16_
    .private_segment_fixed_size: 0
    .sgpr_count:     20
    .sgpr_spill_count: 0
    .symbol:         _Z12scan_combinePKfPKDF16_S0_PDF16_.kd
    .uniform_work_group_size: 1
    .uses_dynamic_stack: false
    .vgpr_count:     66
    .vgpr_spill_count: 0
    .wavefront_size: 64
  - .agpr_count:     0
    .args:
      - .address_space:  global
        .offset:         0
        .size:           8
        .value_kind:     global_buffer
      - .address_space:  global
        .offset:         8
        .size:           8
        .value_kind:     global_buffer
      - .actual_access:  write_only
        .address_space:  global
        .offset:         16
        .size:           8
        .value_kind:     global_buffer
      - .actual_access:  read_only
        .address_space:  global
        .offset:         24
        .size:           8
        .value_kind:     global_buffer
      - .offset:         32
        .size:           4
        .value_kind:     by_value
      - .actual_access:  read_only
        .address_space:  global
        .offset:         40
        .size:           8
        .value_kind:     global_buffer
    .group_segment_fixed_size: 0
    .kernarg_segment_align: 8
    .kernarg_segment_size: 48
    .language:       OpenCL C
    .language_version:
      - 2
      - 0
    .max_flat_workgroup_size: 512
    .name:           _Z11gemm_8phaseILi0ELi16ELi16ELi1024ELi1024ELi4096ELi1EEvPKDF16_S1_PvS2_fPj
    .private_segment_fixed_size: 0
    .sgpr_count:     38
    .sgpr_spill_count: 0
    .symbol:         _Z11gemm_8phaseILi0ELi16ELi16ELi1024ELi1024ELi4096ELi1EEvPKDF16_S1_PvS2_fPj.kd
    .uniform_work_group_size: 1
    .uses_dynamic_stack: false
    .vgpr_count:     236
    .vgpr_spill_count: 0
    .wavefront_size: 64
  - .agpr_count:     0
    .args:
      - .address_space:  global
        .offset:         0
        .size:           8
        .value_kind:     global_buffer
      - .address_space:  global
        .offset:         8
        .size:           8
        .value_kind:     global_buffer
      - .actual_access:  write_only
        .address_space:  global
        .offset:         16
        .size:           8
        .value_kind:     global_buffer
      - .address_space:  global
        .offset:         24
        .size:           8
        .value_kind:     global_buffer
      - .offset:         32
        .size:           4
        .value_kind:     by_value
      - .address_space:  global
        .offset:         40
        .size:           8
        .value_kind:     global_buffer
    .group_segment_fixed_size: 0
    .kernarg_segment_align: 8
    .kernarg_segment_size: 48
    .language:       OpenCL C
    .language_version:
      - 2
      - 0
    .max_flat_workgroup_size: 512
    .name:           _Z11gemm_8phaseILi1ELi16ELi4ELi512ELi2048ELi1024ELi4EEvPKDF16_S1_PvS2_fPj
    .private_segment_fixed_size: 0
    .sgpr_count:     41
    .sgpr_spill_count: 0
    .symbol:         _Z11gemm_8phaseILi1ELi16ELi4ELi512ELi2048ELi1024ELi4EEvPKDF16_S1_PvS2_fPj.kd
    .uniform_work_group_size: 1
    .uses_dynamic_stack: false
    .vgpr_count:     236
    .vgpr_spill_count: 0
    .wavefront_size: 64
  - .agpr_count:     0
    .args:
      - .address_space:  global
        .offset:         0
        .size:           8
        .value_kind:     global_buffer
      - .address_space:  global
        .offset:         8
        .size:           8
        .value_kind:     global_buffer
      - .actual_access:  write_only
        .address_space:  global
        .offset:         16
        .size:           8
        .value_kind:     global_buffer
      - .address_space:  global
        .offset:         24
        .size:           8
        .value_kind:     global_buffer
      - .offset:         32
        .size:           4
        .value_kind:     by_value
      - .address_space:  global
        .offset:         40
        .size:           8
        .value_kind:     global_buffer
    .group_segment_fixed_size: 0
    .kernarg_segment_align: 8
    .kernarg_segment_size: 48
    .language:       OpenCL C
    .language_version:
      - 2
      - 0
    .max_flat_workgroup_size: 512
    .name:           _Z11gemm_8phaseILi2ELi16ELi4ELi512ELi2048ELi1024ELi4EEvPKDF16_S1_PvS2_fPj
    .private_segment_fixed_size: 0
    .sgpr_count:     41
    .sgpr_spill_count: 0
    .symbol:         _Z11gemm_8phaseILi2ELi16ELi4ELi512ELi2048ELi1024ELi4EEvPKDF16_S1_PvS2_fPj.kd
    .uniform_work_group_size: 1
    .uses_dynamic_stack: false
    .vgpr_count:     236
    .vgpr_spill_count: 0
    .wavefront_size: 64
